# prologue weight transposes: the 2-trip load loop unrolled by hand so that an item's 32 loads fly together (one memory round trip per item instead of two)
# speedup vs baseline: 1.0079x; 1.0079x over previous
.LBB0_27:
	s_lshl_b32 s18, s16, 1
	s_lshl_b32 s19, s15, 1
	v_add_u32_e32 v62, s18, v40
	v_add_u32_e32 v60, s19, v35
	v_add_u32_e32 v64, s19, v37
	v_add_u32_e32 v66, s18, v42
	v_add_u32_e32 v68, s19, v41
	v_add_u32_e32 v70, s18, v44
	v_add_u32_e32 v72, s19, v43
	v_add_u32_e32 v74, s18, v46
	v_add_u32_e32 v76, s19, v45
	v_add_u32_e32 v78, s18, v48
	v_add_u32_e32 v80, s19, v47
	v_add_u32_e32 v82, s18, v50
	v_add_u32_e32 v84, s19, v49
	v_add_u32_e32 v86, s18, v52
	v_add_u32_e32 v88, s19, v51
	v_add_u32_e32 v90, s18, v54
	v_ashrrev_i32_e32 v63, 31, v62
	v_ashrrev_i32_e32 v61, 31, v60
	v_ashrrev_i32_e32 v67, 31, v66
	v_ashrrev_i32_e32 v65, 31, v64
	v_ashrrev_i32_e32 v71, 31, v70
	v_ashrrev_i32_e32 v69, 31, v68
	v_ashrrev_i32_e32 v75, 31, v74
	v_ashrrev_i32_e32 v73, 31, v72
	v_ashrrev_i32_e32 v79, 31, v78
	v_ashrrev_i32_e32 v77, 31, v76
	v_ashrrev_i32_e32 v83, 31, v82
	v_ashrrev_i32_e32 v81, 31, v80
	v_ashrrev_i32_e32 v87, 31, v86
	v_ashrrev_i32_e32 v85, 31, v84
	v_ashrrev_i32_e32 v91, 31, v90
	v_ashrrev_i32_e32 v89, 31, v88
	v_lshlrev_b64 v[62:63], 10, v[62:63]
	v_lshlrev_b64 v[60:61], 10, v[60:61]
	v_lshlrev_b64 v[64:65], 10, v[64:65]
	v_lshlrev_b64 v[66:67], 10, v[66:67]
	v_lshlrev_b64 v[68:69], 10, v[68:69]
	v_lshlrev_b64 v[70:71], 10, v[70:71]
	v_lshlrev_b64 v[72:73], 10, v[72:73]
	v_lshlrev_b64 v[74:75], 10, v[74:75]
	v_lshlrev_b64 v[76:77], 10, v[76:77]
	v_lshlrev_b64 v[78:79], 10, v[78:79]
	v_lshlrev_b64 v[80:81], 10, v[80:81]
	v_lshlrev_b64 v[82:83], 10, v[82:83]
	v_lshlrev_b64 v[84:85], 10, v[84:85]
	v_lshlrev_b64 v[86:87], 10, v[86:87]
	v_lshlrev_b64 v[88:89], 10, v[88:89]
	v_lshlrev_b64 v[90:91], 10, v[90:91]
	v_lshl_add_u64 v[62:63], v[38:39], 0, v[62:63]
	v_lshl_add_u64 v[60:61], v[38:39], 0, v[60:61]
	v_lshl_add_u64 v[66:67], v[38:39], 0, v[66:67]
	v_lshl_add_u64 v[64:65], v[38:39], 0, v[64:65]
	v_lshl_add_u64 v[70:71], v[38:39], 0, v[70:71]
	v_lshl_add_u64 v[68:69], v[38:39], 0, v[68:69]
	v_lshl_add_u64 v[74:75], v[38:39], 0, v[74:75]
	v_lshl_add_u64 v[72:73], v[38:39], 0, v[72:73]
	v_lshl_add_u64 v[78:79], v[38:39], 0, v[78:79]
	v_lshl_add_u64 v[76:77], v[38:39], 0, v[76:77]
	v_lshl_add_u64 v[82:83], v[38:39], 0, v[82:83]
	v_lshl_add_u64 v[80:81], v[38:39], 0, v[80:81]
	v_lshl_add_u64 v[86:87], v[38:39], 0, v[86:87]
	v_lshl_add_u64 v[84:85], v[38:39], 0, v[84:85]
	v_lshl_add_u64 v[90:91], v[38:39], 0, v[90:91]
	v_lshl_add_u64 v[88:89], v[38:39], 0, v[88:89]
	global_load_dword v59, v[62:63], off
	global_load_dword v92, v[60:61], off
	global_load_dword v93, v[66:67], off
	global_load_dword v94, v[64:65], off
	global_load_dword v95, v[70:71], off
	global_load_dword v96, v[68:69], off
	global_load_dword v97, v[74:75], off
	global_load_dword v98, v[72:73], off
	global_load_dword v99, v[78:79], off
	global_load_dword v100, v[76:77], off
	global_load_dword v101, v[82:83], off
	global_load_dword v102, v[80:81], off
	global_load_dword v103, v[86:87], off
	global_load_dword v104, v[84:85], off
	global_load_dword v105, v[90:91], off
	global_load_dword v106, v[88:89], off
	s_add_i32 s16, s16, 16
	s_add_i32 s15, s15, 16
	s_add_i32 s17, s17, -16
	s_lshl_b32 s40, s16, 1
	s_lshl_b32 s41, s15, 1
	v_add_u32_e32 v162, s40, v40
	v_add_u32_e32 v160, s41, v35
	v_add_u32_e32 v164, s41, v37
	v_add_u32_e32 v166, s40, v42
	v_add_u32_e32 v168, s41, v41
	v_add_u32_e32 v170, s40, v44
	v_add_u32_e32 v172, s41, v43
	v_add_u32_e32 v174, s40, v46
	v_add_u32_e32 v176, s41, v45
	v_add_u32_e32 v178, s40, v48
	v_add_u32_e32 v180, s41, v47
	v_add_u32_e32 v182, s40, v50
	v_add_u32_e32 v184, s41, v49
	v_add_u32_e32 v186, s40, v52
	v_add_u32_e32 v188, s41, v51
	v_add_u32_e32 v190, s40, v54
	v_ashrrev_i32_e32 v163, 31, v162
	v_ashrrev_i32_e32 v161, 31, v160
	v_ashrrev_i32_e32 v167, 31, v166
	v_ashrrev_i32_e32 v165, 31, v164
	v_ashrrev_i32_e32 v171, 31, v170
	v_ashrrev_i32_e32 v169, 31, v168
	v_ashrrev_i32_e32 v175, 31, v174
	v_ashrrev_i32_e32 v173, 31, v172
	v_ashrrev_i32_e32 v179, 31, v178
	v_ashrrev_i32_e32 v177, 31, v176
	v_ashrrev_i32_e32 v183, 31, v182
	v_ashrrev_i32_e32 v181, 31, v180
	v_ashrrev_i32_e32 v187, 31, v186
	v_ashrrev_i32_e32 v185, 31, v184
	v_ashrrev_i32_e32 v191, 31, v190
	v_ashrrev_i32_e32 v189, 31, v188
	v_lshlrev_b64 v[162:163], 10, v[162:163]
	v_lshlrev_b64 v[160:161], 10, v[160:161]
	v_lshlrev_b64 v[164:165], 10, v[164:165]
	v_lshlrev_b64 v[166:167], 10, v[166:167]
	v_lshlrev_b64 v[168:169], 10, v[168:169]
	v_lshlrev_b64 v[170:171], 10, v[170:171]
	v_lshlrev_b64 v[172:173], 10, v[172:173]
	v_lshlrev_b64 v[174:175], 10, v[174:175]
	v_lshlrev_b64 v[176:177], 10, v[176:177]
	v_lshlrev_b64 v[178:179], 10, v[178:179]
	v_lshlrev_b64 v[180:181], 10, v[180:181]
	v_lshlrev_b64 v[182:183], 10, v[182:183]
	v_lshlrev_b64 v[184:185], 10, v[184:185]
	v_lshlrev_b64 v[186:187], 10, v[186:187]
	v_lshlrev_b64 v[188:189], 10, v[188:189]
	v_lshlrev_b64 v[190:191], 10, v[190:191]
	v_lshl_add_u64 v[162:163], v[38:39], 0, v[162:163]
	v_lshl_add_u64 v[160:161], v[38:39], 0, v[160:161]
	v_lshl_add_u64 v[166:167], v[38:39], 0, v[166:167]
	v_lshl_add_u64 v[164:165], v[38:39], 0, v[164:165]
	v_lshl_add_u64 v[170:171], v[38:39], 0, v[170:171]
	v_lshl_add_u64 v[168:169], v[38:39], 0, v[168:169]
	v_lshl_add_u64 v[174:175], v[38:39], 0, v[174:175]
	v_lshl_add_u64 v[172:173], v[38:39], 0, v[172:173]
	v_lshl_add_u64 v[178:179], v[38:39], 0, v[178:179]
	v_lshl_add_u64 v[176:177], v[38:39], 0, v[176:177]
	v_lshl_add_u64 v[182:183], v[38:39], 0, v[182:183]
	v_lshl_add_u64 v[180:181], v[38:39], 0, v[180:181]
	v_lshl_add_u64 v[186:187], v[38:39], 0, v[186:187]
	v_lshl_add_u64 v[184:185], v[38:39], 0, v[184:185]
	v_lshl_add_u64 v[190:191], v[38:39], 0, v[190:191]
	v_lshl_add_u64 v[188:189], v[38:39], 0, v[188:189]
	global_load_dword v159, v[162:163], off
	global_load_dword v192, v[160:161], off
	global_load_dword v193, v[166:167], off
	global_load_dword v194, v[164:165], off
	global_load_dword v195, v[170:171], off
	global_load_dword v196, v[168:169], off
	global_load_dword v197, v[174:175], off
	global_load_dword v198, v[172:173], off
	global_load_dword v199, v[178:179], off
	global_load_dword v200, v[176:177], off
	global_load_dword v201, v[182:183], off
	global_load_dword v202, v[180:181], off
	global_load_dword v203, v[186:187], off
	global_load_dword v204, v[184:185], off
	global_load_dword v205, v[190:191], off
	global_load_dword v206, v[188:189], off
	s_add_i32 s16, s16, 16
	s_add_i32 s15, s15, 16
	s_add_i32 s17, s17, -16
	v_add_u32_e32 v60, s18, v0
	v_add_u32_e32 v62, s19, v1
	v_add_u32_e32 v66, s19, v21
	v_add_u32_e32 v64, s18, v22
	v_add_u32_e32 v70, s19, v23
	v_add_u32_e32 v68, s18, v24
	v_add_u32_e32 v74, s19, v25
	v_add_u32_e32 v72, s18, v26
	v_add_u32_e32 v78, s19, v27
	v_add_u32_e32 v76, s18, v28
	v_add_u32_e32 v82, s19, v29
	v_add_u32_e32 v80, s18, v30
	v_add_u32_e32 v86, s19, v31
	v_add_u32_e32 v84, s18, v32
	v_add_u32_e32 v90, s19, v33
	v_add_u32_e32 v88, s18, v34
	v_mad_u64_u32 v[60:61], s[18:19], v60, s24, v[20:21]
	v_mad_u64_u32 v[62:63], s[18:19], v62, s24, v[20:21]
	v_mad_u64_u32 v[64:65], s[18:19], v64, s24, v[20:21]
	v_mad_u64_u32 v[66:67], s[18:19], v66, s24, v[20:21]
	v_mad_u64_u32 v[68:69], s[18:19], v68, s24, v[20:21]
	v_mad_u64_u32 v[70:71], s[18:19], v70, s24, v[20:21]
	v_mad_u64_u32 v[72:73], s[18:19], v72, s24, v[20:21]
	v_mad_u64_u32 v[74:75], s[18:19], v74, s24, v[20:21]
	v_mad_u64_u32 v[76:77], s[18:19], v76, s24, v[20:21]
	v_mad_u64_u32 v[78:79], s[18:19], v78, s24, v[20:21]
	v_mad_u64_u32 v[80:81], s[18:19], v80, s24, v[20:21]
	v_mad_u64_u32 v[82:83], s[18:19], v82, s24, v[20:21]
	v_mad_u64_u32 v[84:85], s[18:19], v84, s24, v[20:21]
	v_mad_u64_u32 v[86:87], s[18:19], v86, s24, v[20:21]
	v_mad_u64_u32 v[88:89], s[18:19], v88, s24, v[20:21]
	v_mad_u64_u32 v[90:91], s[18:19], v90, s24, v[20:21]
	s_waitcnt vmcnt(31)
	ds_write_b32 v60, v59
	s_waitcnt vmcnt(30)
	ds_write_b32 v62, v92
	s_waitcnt vmcnt(29)
	ds_write_b32 v64, v93
	s_waitcnt vmcnt(28)
	ds_write_b32 v66, v94
	s_waitcnt vmcnt(27)
	ds_write_b32 v68, v95
	s_waitcnt vmcnt(26)
	ds_write_b32 v70, v96
	s_waitcnt vmcnt(25)
	ds_write_b32 v72, v97
	s_waitcnt vmcnt(24)
	ds_write_b32 v74, v98
	s_waitcnt vmcnt(23)
	ds_write_b32 v76, v99
	s_waitcnt vmcnt(22)
	ds_write_b32 v78, v100
	s_waitcnt vmcnt(21)
	ds_write_b32 v80, v101
	s_waitcnt vmcnt(20)
	ds_write_b32 v82, v102
	s_waitcnt vmcnt(19)
	ds_write_b32 v84, v103
	s_waitcnt vmcnt(18)
	ds_write_b32 v86, v104
	s_waitcnt vmcnt(17)
	ds_write_b32 v88, v105
	s_waitcnt vmcnt(16)
	ds_write_b32 v90, v106
	v_add_u32_e32 v160, s40, v0
	v_add_u32_e32 v162, s41, v1
	v_add_u32_e32 v166, s41, v21
	v_add_u32_e32 v164, s40, v22
	v_add_u32_e32 v170, s41, v23
	v_add_u32_e32 v168, s40, v24
	v_add_u32_e32 v174, s41, v25
	v_add_u32_e32 v172, s40, v26
	v_add_u32_e32 v178, s41, v27
	v_add_u32_e32 v176, s40, v28
	v_add_u32_e32 v182, s41, v29
	v_add_u32_e32 v180, s40, v30
	v_add_u32_e32 v186, s41, v31
	v_add_u32_e32 v184, s40, v32
	v_add_u32_e32 v190, s41, v33
	v_add_u32_e32 v188, s40, v34
	v_mad_u64_u32 v[160:161], s[40:41], v160, s24, v[20:21]
	v_mad_u64_u32 v[162:163], s[40:41], v162, s24, v[20:21]
	v_mad_u64_u32 v[164:165], s[40:41], v164, s24, v[20:21]
	v_mad_u64_u32 v[166:167], s[40:41], v166, s24, v[20:21]
	v_mad_u64_u32 v[168:169], s[40:41], v168, s24, v[20:21]
	v_mad_u64_u32 v[170:171], s[40:41], v170, s24, v[20:21]
	v_mad_u64_u32 v[172:173], s[40:41], v172, s24, v[20:21]
	v_mad_u64_u32 v[174:175], s[40:41], v174, s24, v[20:21]
	v_mad_u64_u32 v[176:177], s[40:41], v176, s24, v[20:21]
	v_mad_u64_u32 v[178:179], s[40:41], v178, s24, v[20:21]
	v_mad_u64_u32 v[180:181], s[40:41], v180, s24, v[20:21]
	v_mad_u64_u32 v[182:183], s[40:41], v182, s24, v[20:21]
	v_mad_u64_u32 v[184:185], s[40:41], v184, s24, v[20:21]
	v_mad_u64_u32 v[186:187], s[40:41], v186, s24, v[20:21]
	v_mad_u64_u32 v[188:189], s[40:41], v188, s24, v[20:21]
	v_mad_u64_u32 v[190:191], s[40:41], v190, s24, v[20:21]
	s_waitcnt vmcnt(15)
	ds_write_b32 v160, v159
	s_waitcnt vmcnt(14)
	ds_write_b32 v162, v192
	s_waitcnt vmcnt(13)
	ds_write_b32 v164, v193
	s_waitcnt vmcnt(12)
	ds_write_b32 v166, v194
	s_waitcnt vmcnt(11)
	ds_write_b32 v168, v195
	s_waitcnt vmcnt(10)
	ds_write_b32 v170, v196
	s_waitcnt vmcnt(9)
	ds_write_b32 v172, v197
	s_waitcnt vmcnt(8)
	ds_write_b32 v174, v198
	s_waitcnt vmcnt(7)
	ds_write_b32 v176, v199
	s_waitcnt vmcnt(6)
	ds_write_b32 v178, v200
	s_waitcnt vmcnt(5)
	ds_write_b32 v180, v201
	s_waitcnt vmcnt(4)
	ds_write_b32 v182, v202
	s_waitcnt vmcnt(3)
	ds_write_b32 v184, v203
	s_waitcnt vmcnt(2)
	ds_write_b32 v186, v204
	s_waitcnt vmcnt(1)
	ds_write_b32 v188, v205
	s_waitcnt vmcnt(0)
	ds_write_b32 v190, v206
	s_waitcnt lgkmcnt(0)
	s_lshl_b32 s12, s12, 19
	ds_read2_b32 v[42:43], v55 offset1:8
	s_add_u32 s12, s22, s12
	ds_read2_b32 v[46:47], v55 offset0:33 offset1:41
	s_addc_u32 s15, s23, 0
	s_lshl_b32 s2, s2, 8
	s_or_b32 s2, s14, s2
	s_lshl_b32 s13, s13, 1
	ds_read2_b32 v[48:49], v55 offset0:66 offset1:74
	s_add_u32 s12, s12, s13
	ds_read2_b32 v[50:51], v55 offset0:99 offset1:107
	s_addc_u32 s13, s15, 0
	v_mov_b32_e32 v37, v3
	s_waitcnt lgkmcnt(3)
	v_bfe_u32 v35, v42, 16, 1
	v_lshl_add_u64 v[44:45], s[12:13], 0, v[36:37]
	v_add3_u32 v35, v42, v35, s26
	s_waitcnt lgkmcnt(2)
	v_bfe_u32 v37, v46, 16, 1
	ds_read2_b32 v[60:61], v55 offset0:132 offset1:140
	v_lshrrev_b32_e32 v35, 16, v35
	v_add3_u32 v37, v46, v37, s26
	ds_read2_b32 v[62:63], v55 offset0:165 offset1:173
	v_and_or_b32 v38, v37, s27, v35
	s_waitcnt lgkmcnt(3)
	v_bfe_u32 v35, v48, 16, 1
	v_add3_u32 v35, v48, v35, s26
	s_waitcnt lgkmcnt(2)
	v_bfe_u32 v37, v50, 16, 1
	ds_read2_b32 v[64:65], v55 offset0:198 offset1:206
	v_lshrrev_b32_e32 v35, 16, v35
	v_add3_u32 v37, v50, v37, s26
	ds_read2_b32 v[66:67], v55 offset0:231 offset1:239
	v_and_or_b32 v39, v37, s27, v35
	s_waitcnt lgkmcnt(3)
	v_bfe_u32 v35, v60, 16, 1
	v_add3_u32 v35, v60, v35, s26
	s_waitcnt lgkmcnt(2)
	v_bfe_u32 v37, v62, 16, 1
	v_lshrrev_b32_e32 v35, 16, v35
	v_add3_u32 v37, v62, v37, s26
	v_and_or_b32 v40, v37, s27, v35
	s_waitcnt lgkmcnt(1)
	v_bfe_u32 v35, v64, 16, 1
	v_add3_u32 v35, v64, v35, s26
	s_waitcnt lgkmcnt(0)
	v_bfe_u32 v37, v66, 16, 1
	v_lshrrev_b32_e32 v35, 16, v35
	v_add3_u32 v37, v66, v37, s26
	v_add_u32_e32 v68, s2, v53
	v_and_or_b32 v41, v37, s27, v35
	v_ashrrev_i32_e32 v69, 31, v68
	v_bfe_u32 v35, v43, 16, 1
	v_lshlrev_b64 v[68:69], 9, v[68:69]
	v_add3_u32 v35, v43, v35, s26
	v_bfe_u32 v37, v47, 16, 1
	v_lshl_add_u64 v[68:69], v[44:45], 0, v[68:69]
	v_lshrrev_b32_e32 v35, 16, v35
	v_add3_u32 v37, v47, v37, s26
	global_store_dwordx4 v[68:69], v[38:41], off
	v_add_u32_e32 v42, s2, v56
	v_ashrrev_i32_e32 v43, 31, v42
	v_and_or_b32 v38, v37, s27, v35
	v_bfe_u32 v35, v49, 16, 1
	v_add3_u32 v35, v49, v35, s26
	v_bfe_u32 v37, v51, 16, 1
	v_lshrrev_b32_e32 v35, 16, v35
	v_add3_u32 v37, v51, v37, s26
	v_and_or_b32 v39, v37, s27, v35
	v_bfe_u32 v35, v61, 16, 1
	v_add3_u32 v35, v61, v35, s26
	v_bfe_u32 v37, v63, 16, 1
	v_lshrrev_b32_e32 v35, 16, v35
	v_add3_u32 v37, v63, v37, s26
	v_and_or_b32 v40, v37, s27, v35
	v_bfe_u32 v35, v65, 16, 1
	v_add3_u32 v35, v65, v35, s26
	v_bfe_u32 v37, v67, 16, 1
	v_lshrrev_b32_e32 v35, 16, v35
	v_add3_u32 v37, v67, v37, s26
	v_lshlrev_b64 v[42:43], 9, v[42:43]
	v_and_or_b32 v41, v37, s27, v35
	ds_read2_b32 v[46:47], v55 offset0:16 offset1:24
	v_lshl_add_u64 v[42:43], v[44:45], 0, v[42:43]
	global_store_dwordx4 v[42:43], v[38:41], off
	ds_read2_b32 v[42:43], v55 offset0:49 offset1:57
	ds_read2_b32 v[48:49], v55 offset0:82 offset1:90
	ds_read2_b32 v[50:51], v55 offset0:115 offset1:123
	s_waitcnt lgkmcnt(3)
	v_bfe_u32 v35, v46, 16, 1
	v_add3_u32 v35, v46, v35, s26
	s_waitcnt lgkmcnt(2)
	v_bfe_u32 v37, v42, 16, 1
	ds_read2_b32 v[60:61], v55 offset0:148 offset1:156
	v_lshrrev_b32_e32 v35, 16, v35
	v_add3_u32 v37, v42, v37, s26
	ds_read2_b32 v[62:63], v55 offset0:181 offset1:189
	v_and_or_b32 v38, v37, s27, v35
	s_waitcnt lgkmcnt(3)
	v_bfe_u32 v35, v48, 16, 1
	v_add3_u32 v35, v48, v35, s26
	s_waitcnt lgkmcnt(2)
	v_bfe_u32 v37, v50, 16, 1
	ds_read2_b32 v[64:65], v55 offset0:214 offset1:222
	v_lshrrev_b32_e32 v35, 16, v35
	v_add3_u32 v37, v50, v37, s26
	ds_read2_b32 v[66:67], v55 offset0:247 offset1:255
	v_and_or_b32 v39, v37, s27, v35
	s_waitcnt lgkmcnt(3)
	v_bfe_u32 v35, v60, 16, 1
	v_add3_u32 v35, v60, v35, s26
	s_waitcnt lgkmcnt(2)
	v_bfe_u32 v37, v62, 16, 1
	v_lshrrev_b32_e32 v35, 16, v35
	v_add3_u32 v37, v62, v37, s26
	v_and_or_b32 v40, v37, s27, v35
	s_waitcnt lgkmcnt(1)
	v_bfe_u32 v35, v64, 16, 1
	v_add3_u32 v35, v64, v35, s26
	s_waitcnt lgkmcnt(0)
	v_bfe_u32 v37, v66, 16, 1
	v_lshrrev_b32_e32 v35, 16, v35
	v_add3_u32 v37, v66, v37, s26
	v_add_u32_e32 v68, s2, v57
	v_and_or_b32 v41, v37, s27, v35
	v_ashrrev_i32_e32 v69, 31, v68
	v_bfe_u32 v35, v47, 16, 1
	v_lshlrev_b64 v[68:69], 9, v[68:69]
	v_add3_u32 v35, v47, v35, s26
	v_bfe_u32 v37, v43, 16, 1
	v_lshl_add_u64 v[68:69], v[44:45], 0, v[68:69]
	v_lshrrev_b32_e32 v35, 16, v35
	v_add3_u32 v37, v43, v37, s26
	global_store_dwordx4 v[68:69], v[38:41], off
	v_add_u32_e32 v42, s2, v58
	v_ashrrev_i32_e32 v43, 31, v42
	v_and_or_b32 v38, v37, s27, v35
	v_bfe_u32 v35, v49, 16, 1
	v_add3_u32 v35, v49, v35, s26
	v_bfe_u32 v37, v51, 16, 1
	v_lshrrev_b32_e32 v35, 16, v35
	v_add3_u32 v37, v51, v37, s26
	v_and_or_b32 v39, v37, s27, v35
	v_bfe_u32 v35, v61, 16, 1
	v_add3_u32 v35, v61, v35, s26
	v_bfe_u32 v37, v63, 16, 1
	v_lshrrev_b32_e32 v35, 16, v35
	v_add3_u32 v37, v63, v37, s26
	v_and_or_b32 v40, v37, s27, v35
	v_bfe_u32 v35, v65, 16, 1
	v_add3_u32 v35, v65, v35, s26
	v_bfe_u32 v37, v67, 16, 1
	v_lshrrev_b32_e32 v35, 16, v35
	v_add3_u32 v37, v67, v37, s26
	v_lshlrev_b64 v[42:43], 9, v[42:43]
	v_and_or_b32 v41, v37, s27, v35
	v_lshl_add_u64 v[42:43], v[44:45], 0, v[42:43]
	global_store_dwordx4 v[42:43], v[38:41], off
	s_waitcnt lgkmcnt(0)
	s_mov_b64 s[12:13], 0

.LBB0_31:
	s_lshl_b32 s16, s2, 1
	s_lshl_b32 s17, s14, 1
	v_add_u32_e32 v62, s16, v40
	v_add_u32_e32 v60, s17, v35
	v_add_u32_e32 v64, s17, v37
	v_add_u32_e32 v66, s16, v42
	v_add_u32_e32 v68, s17, v41
	v_add_u32_e32 v70, s16, v44
	v_add_u32_e32 v72, s17, v43
	v_add_u32_e32 v74, s16, v46
	v_add_u32_e32 v76, s17, v45
	v_add_u32_e32 v78, s16, v48
	v_add_u32_e32 v80, s17, v47
	v_add_u32_e32 v82, s16, v50
	v_add_u32_e32 v84, s17, v49
	v_add_u32_e32 v86, s16, v52
	v_add_u32_e32 v88, s17, v51
	v_add_u32_e32 v90, s16, v54
	v_ashrrev_i32_e32 v63, 31, v62
	v_ashrrev_i32_e32 v61, 31, v60
	v_ashrrev_i32_e32 v67, 31, v66
	v_ashrrev_i32_e32 v65, 31, v64
	v_ashrrev_i32_e32 v71, 31, v70
	v_ashrrev_i32_e32 v69, 31, v68
	v_ashrrev_i32_e32 v75, 31, v74
	v_ashrrev_i32_e32 v73, 31, v72
	v_ashrrev_i32_e32 v79, 31, v78
	v_ashrrev_i32_e32 v77, 31, v76
	v_ashrrev_i32_e32 v83, 31, v82
	v_ashrrev_i32_e32 v81, 31, v80
	v_ashrrev_i32_e32 v87, 31, v86
	v_ashrrev_i32_e32 v85, 31, v84
	v_ashrrev_i32_e32 v91, 31, v90
	v_ashrrev_i32_e32 v89, 31, v88
	v_lshlrev_b64 v[62:63], 12, v[62:63]
	v_lshlrev_b64 v[60:61], 12, v[60:61]
	v_lshlrev_b64 v[64:65], 12, v[64:65]
	v_lshlrev_b64 v[66:67], 12, v[66:67]
	v_lshlrev_b64 v[68:69], 12, v[68:69]
	v_lshlrev_b64 v[70:71], 12, v[70:71]
	v_lshlrev_b64 v[72:73], 12, v[72:73]
	v_lshlrev_b64 v[74:75], 12, v[74:75]
	v_lshlrev_b64 v[76:77], 12, v[76:77]
	v_lshlrev_b64 v[78:79], 12, v[78:79]
	v_lshlrev_b64 v[80:81], 12, v[80:81]
	v_lshlrev_b64 v[82:83], 12, v[82:83]
	v_lshlrev_b64 v[84:85], 12, v[84:85]
	v_lshlrev_b64 v[86:87], 12, v[86:87]
	v_lshlrev_b64 v[88:89], 12, v[88:89]
	v_lshlrev_b64 v[90:91], 12, v[90:91]
	v_lshl_add_u64 v[62:63], v[38:39], 0, v[62:63]
	v_lshl_add_u64 v[60:61], v[38:39], 0, v[60:61]
	v_lshl_add_u64 v[66:67], v[38:39], 0, v[66:67]
	v_lshl_add_u64 v[64:65], v[38:39], 0, v[64:65]
	v_lshl_add_u64 v[70:71], v[38:39], 0, v[70:71]
	v_lshl_add_u64 v[68:69], v[38:39], 0, v[68:69]
	v_lshl_add_u64 v[74:75], v[38:39], 0, v[74:75]
	v_lshl_add_u64 v[72:73], v[38:39], 0, v[72:73]
	v_lshl_add_u64 v[78:79], v[38:39], 0, v[78:79]
	v_lshl_add_u64 v[76:77], v[38:39], 0, v[76:77]
	v_lshl_add_u64 v[82:83], v[38:39], 0, v[82:83]
	v_lshl_add_u64 v[80:81], v[38:39], 0, v[80:81]
	v_lshl_add_u64 v[86:87], v[38:39], 0, v[86:87]
	v_lshl_add_u64 v[84:85], v[38:39], 0, v[84:85]
	v_lshl_add_u64 v[90:91], v[38:39], 0, v[90:91]
	v_lshl_add_u64 v[88:89], v[38:39], 0, v[88:89]
	global_load_dword v59, v[62:63], off
	global_load_dword v92, v[60:61], off
	global_load_dword v93, v[66:67], off
	global_load_dword v94, v[64:65], off
	global_load_dword v95, v[70:71], off
	global_load_dword v96, v[68:69], off
	global_load_dword v97, v[74:75], off
	global_load_dword v98, v[72:73], off
	global_load_dword v99, v[78:79], off
	global_load_dword v100, v[76:77], off
	global_load_dword v101, v[82:83], off
	global_load_dword v102, v[80:81], off
	global_load_dword v103, v[86:87], off
	global_load_dword v104, v[84:85], off
	global_load_dword v105, v[90:91], off
	global_load_dword v106, v[88:89], off
	s_add_i32 s2, s2, 16
	s_add_i32 s14, s14, 16
	s_add_i32 s15, s15, -16
	s_lshl_b32 s40, s2, 1
	s_lshl_b32 s41, s14, 1
	v_add_u32_e32 v162, s40, v40
	v_add_u32_e32 v160, s41, v35
	v_add_u32_e32 v164, s41, v37
	v_add_u32_e32 v166, s40, v42
	v_add_u32_e32 v168, s41, v41
	v_add_u32_e32 v170, s40, v44
	v_add_u32_e32 v172, s41, v43
	v_add_u32_e32 v174, s40, v46
	v_add_u32_e32 v176, s41, v45
	v_add_u32_e32 v178, s40, v48
	v_add_u32_e32 v180, s41, v47
	v_add_u32_e32 v182, s40, v50
	v_add_u32_e32 v184, s41, v49
	v_add_u32_e32 v186, s40, v52
	v_add_u32_e32 v188, s41, v51
	v_add_u32_e32 v190, s40, v54
	v_ashrrev_i32_e32 v163, 31, v162
	v_ashrrev_i32_e32 v161, 31, v160
	v_ashrrev_i32_e32 v167, 31, v166
	v_ashrrev_i32_e32 v165, 31, v164
	v_ashrrev_i32_e32 v171, 31, v170
	v_ashrrev_i32_e32 v169, 31, v168
	v_ashrrev_i32_e32 v175, 31, v174
	v_ashrrev_i32_e32 v173, 31, v172
	v_ashrrev_i32_e32 v179, 31, v178
	v_ashrrev_i32_e32 v177, 31, v176
	v_ashrrev_i32_e32 v183, 31, v182
	v_ashrrev_i32_e32 v181, 31, v180
	v_ashrrev_i32_e32 v187, 31, v186
	v_ashrrev_i32_e32 v185, 31, v184
	v_ashrrev_i32_e32 v191, 31, v190
	v_ashrrev_i32_e32 v189, 31, v188
	v_lshlrev_b64 v[162:163], 12, v[162:163]
	v_lshlrev_b64 v[160:161], 12, v[160:161]
	v_lshlrev_b64 v[164:165], 12, v[164:165]
	v_lshlrev_b64 v[166:167], 12, v[166:167]
	v_lshlrev_b64 v[168:169], 12, v[168:169]
	v_lshlrev_b64 v[170:171], 12, v[170:171]
	v_lshlrev_b64 v[172:173], 12, v[172:173]
	v_lshlrev_b64 v[174:175], 12, v[174:175]
	v_lshlrev_b64 v[176:177], 12, v[176:177]
	v_lshlrev_b64 v[178:179], 12, v[178:179]
	v_lshlrev_b64 v[180:181], 12, v[180:181]
	v_lshlrev_b64 v[182:183], 12, v[182:183]
	v_lshlrev_b64 v[184:185], 12, v[184:185]
	v_lshlrev_b64 v[186:187], 12, v[186:187]
	v_lshlrev_b64 v[188:189], 12, v[188:189]
	v_lshlrev_b64 v[190:191], 12, v[190:191]
	v_lshl_add_u64 v[162:163], v[38:39], 0, v[162:163]
	v_lshl_add_u64 v[160:161], v[38:39], 0, v[160:161]
	v_lshl_add_u64 v[166:167], v[38:39], 0, v[166:167]
	v_lshl_add_u64 v[164:165], v[38:39], 0, v[164:165]
	v_lshl_add_u64 v[170:171], v[38:39], 0, v[170:171]
	v_lshl_add_u64 v[168:169], v[38:39], 0, v[168:169]
	v_lshl_add_u64 v[174:175], v[38:39], 0, v[174:175]
	v_lshl_add_u64 v[172:173], v[38:39], 0, v[172:173]
	v_lshl_add_u64 v[178:179], v[38:39], 0, v[178:179]
	v_lshl_add_u64 v[176:177], v[38:39], 0, v[176:177]
	v_lshl_add_u64 v[182:183], v[38:39], 0, v[182:183]
	v_lshl_add_u64 v[180:181], v[38:39], 0, v[180:181]
	v_lshl_add_u64 v[186:187], v[38:39], 0, v[186:187]
	v_lshl_add_u64 v[184:185], v[38:39], 0, v[184:185]
	v_lshl_add_u64 v[190:191], v[38:39], 0, v[190:191]
	v_lshl_add_u64 v[188:189], v[38:39], 0, v[188:189]
	global_load_dword v159, v[162:163], off
	global_load_dword v192, v[160:161], off
	global_load_dword v193, v[166:167], off
	global_load_dword v194, v[164:165], off
	global_load_dword v195, v[170:171], off
	global_load_dword v196, v[168:169], off
	global_load_dword v197, v[174:175], off
	global_load_dword v198, v[172:173], off
	global_load_dword v199, v[178:179], off
	global_load_dword v200, v[176:177], off
	global_load_dword v201, v[182:183], off
	global_load_dword v202, v[180:181], off
	global_load_dword v203, v[186:187], off
	global_load_dword v204, v[184:185], off
	global_load_dword v205, v[190:191], off
	global_load_dword v206, v[188:189], off
	s_add_i32 s2, s2, 16
	s_add_i32 s14, s14, 16
	s_add_i32 s15, s15, -16
	v_add_u32_e32 v60, s16, v0
	v_add_u32_e32 v62, s17, v1
	v_add_u32_e32 v66, s17, v21
	v_add_u32_e32 v64, s16, v22
	v_add_u32_e32 v70, s17, v23
	v_add_u32_e32 v68, s16, v24
	v_add_u32_e32 v74, s17, v25
	v_add_u32_e32 v72, s16, v26
	v_add_u32_e32 v78, s17, v27
	v_add_u32_e32 v76, s16, v28
	v_add_u32_e32 v82, s17, v29
	v_add_u32_e32 v80, s16, v30
	v_add_u32_e32 v86, s17, v31
	v_add_u32_e32 v84, s16, v32
	v_add_u32_e32 v90, s17, v33
	v_add_u32_e32 v88, s16, v34
	v_mad_u64_u32 v[60:61], s[16:17], v60, s24, v[20:21]
	v_mad_u64_u32 v[62:63], s[16:17], v62, s24, v[20:21]
	v_mad_u64_u32 v[64:65], s[16:17], v64, s24, v[20:21]
	v_mad_u64_u32 v[66:67], s[16:17], v66, s24, v[20:21]
	v_mad_u64_u32 v[68:69], s[16:17], v68, s24, v[20:21]
	v_mad_u64_u32 v[70:71], s[16:17], v70, s24, v[20:21]
	v_mad_u64_u32 v[72:73], s[16:17], v72, s24, v[20:21]
	v_mad_u64_u32 v[74:75], s[16:17], v74, s24, v[20:21]
	v_mad_u64_u32 v[76:77], s[16:17], v76, s24, v[20:21]
	v_mad_u64_u32 v[78:79], s[16:17], v78, s24, v[20:21]
	v_mad_u64_u32 v[80:81], s[16:17], v80, s24, v[20:21]
	v_mad_u64_u32 v[82:83], s[16:17], v82, s24, v[20:21]
	v_mad_u64_u32 v[84:85], s[16:17], v84, s24, v[20:21]
	v_mad_u64_u32 v[86:87], s[16:17], v86, s24, v[20:21]
	v_mad_u64_u32 v[88:89], s[16:17], v88, s24, v[20:21]
	v_mad_u64_u32 v[90:91], s[16:17], v90, s24, v[20:21]
	s_waitcnt vmcnt(31)
	ds_write_b32 v60, v59
	s_waitcnt vmcnt(30)
	ds_write_b32 v62, v92
	s_waitcnt vmcnt(29)
	ds_write_b32 v64, v93
	s_waitcnt vmcnt(28)
	ds_write_b32 v66, v94
	s_waitcnt vmcnt(27)
	ds_write_b32 v68, v95
	s_waitcnt vmcnt(26)
	ds_write_b32 v70, v96
	s_waitcnt vmcnt(25)
	ds_write_b32 v72, v97
	s_waitcnt vmcnt(24)
	ds_write_b32 v74, v98
	s_waitcnt vmcnt(23)
	ds_write_b32 v76, v99
	s_waitcnt vmcnt(22)
	ds_write_b32 v78, v100
	s_waitcnt vmcnt(21)
	ds_write_b32 v80, v101
	s_waitcnt vmcnt(20)
	ds_write_b32 v82, v102
	s_waitcnt vmcnt(19)
	ds_write_b32 v84, v103
	s_waitcnt vmcnt(18)
	ds_write_b32 v86, v104
	s_waitcnt vmcnt(17)
	ds_write_b32 v88, v105
	s_waitcnt vmcnt(16)
	ds_write_b32 v90, v106
	v_add_u32_e32 v160, s40, v0
	v_add_u32_e32 v162, s41, v1
	v_add_u32_e32 v166, s41, v21
	v_add_u32_e32 v164, s40, v22
	v_add_u32_e32 v170, s41, v23
	v_add_u32_e32 v168, s40, v24
	v_add_u32_e32 v174, s41, v25
	v_add_u32_e32 v172, s40, v26
	v_add_u32_e32 v178, s41, v27
	v_add_u32_e32 v176, s40, v28
	v_add_u32_e32 v182, s41, v29
	v_add_u32_e32 v180, s40, v30
	v_add_u32_e32 v186, s41, v31
	v_add_u32_e32 v184, s40, v32
	v_add_u32_e32 v190, s41, v33
	v_add_u32_e32 v188, s40, v34
	v_mad_u64_u32 v[160:161], s[40:41], v160, s24, v[20:21]
	v_mad_u64_u32 v[162:163], s[40:41], v162, s24, v[20:21]
	v_mad_u64_u32 v[164:165], s[40:41], v164, s24, v[20:21]
	v_mad_u64_u32 v[166:167], s[40:41], v166, s24, v[20:21]
	v_mad_u64_u32 v[168:169], s[40:41], v168, s24, v[20:21]
	v_mad_u64_u32 v[170:171], s[40:41], v170, s24, v[20:21]
	v_mad_u64_u32 v[172:173], s[40:41], v172, s24, v[20:21]
	v_mad_u64_u32 v[174:175], s[40:41], v174, s24, v[20:21]
	v_mad_u64_u32 v[176:177], s[40:41], v176, s24, v[20:21]
	v_mad_u64_u32 v[178:179], s[40:41], v178, s24, v[20:21]
	v_mad_u64_u32 v[180:181], s[40:41], v180, s24, v[20:21]
	v_mad_u64_u32 v[182:183], s[40:41], v182, s24, v[20:21]
	v_mad_u64_u32 v[184:185], s[40:41], v184, s24, v[20:21]
	v_mad_u64_u32 v[186:187], s[40:41], v186, s24, v[20:21]
	v_mad_u64_u32 v[188:189], s[40:41], v188, s24, v[20:21]
	v_mad_u64_u32 v[190:191], s[40:41], v190, s24, v[20:21]
	s_waitcnt vmcnt(15)
	ds_write_b32 v160, v159
	s_waitcnt vmcnt(14)
	ds_write_b32 v162, v192
	s_waitcnt vmcnt(13)
	ds_write_b32 v164, v193
	s_waitcnt vmcnt(12)
	ds_write_b32 v166, v194
	s_waitcnt vmcnt(11)
	ds_write_b32 v168, v195
	s_waitcnt vmcnt(10)
	ds_write_b32 v170, v196
	s_waitcnt vmcnt(9)
	ds_write_b32 v172, v197
	s_waitcnt vmcnt(8)
	ds_write_b32 v174, v198
	s_waitcnt vmcnt(7)
	ds_write_b32 v176, v199
	s_waitcnt vmcnt(6)
	ds_write_b32 v178, v200
	s_waitcnt vmcnt(5)
	ds_write_b32 v180, v201
	s_waitcnt vmcnt(4)
	ds_write_b32 v182, v202
	s_waitcnt vmcnt(3)
	ds_write_b32 v184, v203
	s_waitcnt vmcnt(2)
	ds_write_b32 v186, v204
	s_waitcnt vmcnt(1)
	ds_write_b32 v188, v205
	s_waitcnt vmcnt(0)
	ds_write_b32 v190, v206
	s_waitcnt lgkmcnt(0)
	ds_read2_b32 v[42:43], v55 offset1:8
	ds_read2_b32 v[46:47], v55 offset0:33 offset1:41
	ds_read2_b32 v[48:49], v55 offset0:66 offset1:74
	ds_read2_b32 v[50:51], v55 offset0:99 offset1:107
	ds_read2_b32 v[60:61], v55 offset0:132 offset1:140
	ds_read2_b32 v[62:63], v55 offset0:165 offset1:173
	s_waitcnt lgkmcnt(5)
	v_bfe_u32 v35, v42, 16, 1
	v_add3_u32 v35, v42, v35, s26
	s_waitcnt lgkmcnt(4)
	v_bfe_u32 v37, v46, 16, 1
	v_lshrrev_b32_e32 v35, 16, v35
	v_add3_u32 v37, v46, v37, s26
	v_and_or_b32 v38, v37, s27, v35
	s_waitcnt lgkmcnt(3)
	v_bfe_u32 v35, v48, 16, 1
	v_add3_u32 v35, v48, v35, s26
	s_waitcnt lgkmcnt(2)
	v_bfe_u32 v37, v50, 16, 1
	ds_read2_b32 v[64:65], v55 offset0:198 offset1:206
	v_lshrrev_b32_e32 v35, 16, v35
	v_add3_u32 v37, v50, v37, s26
	ds_read2_b32 v[66:67], v55 offset0:231 offset1:239
	v_and_or_b32 v39, v37, s27, v35
	s_waitcnt lgkmcnt(3)
	v_bfe_u32 v35, v60, 16, 1
	v_add3_u32 v35, v60, v35, s26
	s_waitcnt lgkmcnt(2)
	v_bfe_u32 v37, v62, 16, 1
	v_lshrrev_b32_e32 v35, 16, v35
	v_add3_u32 v37, v62, v37, s26
	v_and_or_b32 v40, v37, s27, v35
	s_waitcnt lgkmcnt(1)
	v_bfe_u32 v35, v64, 16, 1
	v_add3_u32 v35, v64, v35, s26
	s_waitcnt lgkmcnt(0)
	v_bfe_u32 v37, v66, 16, 1
	v_lshrrev_b32_e32 v35, 16, v35
	v_add3_u32 v37, v66, v37, s26
	v_add_u32_e32 v68, s12, v53
	s_lshl_b32 s2, s13, 1
	v_and_or_b32 v41, v37, s27, v35
	v_ashrrev_i32_e32 v69, 31, v68
	v_bfe_u32 v35, v43, 16, 1
	v_lshl_add_u64 v[44:45], v[6:7], 0, s[2:3]
	v_lshlrev_b64 v[68:69], 11, v[68:69]
	v_add3_u32 v35, v43, v35, s26
	v_bfe_u32 v37, v47, 16, 1
	v_lshl_add_u64 v[68:69], v[44:45], 0, v[68:69]
	v_lshrrev_b32_e32 v35, 16, v35
	v_add3_u32 v37, v47, v37, s26
	global_store_dwordx4 v[68:69], v[38:41], off
	v_add_u32_e32 v42, s12, v56
	v_ashrrev_i32_e32 v43, 31, v42
	v_and_or_b32 v38, v37, s27, v35
	v_bfe_u32 v35, v49, 16, 1
	v_add3_u32 v35, v49, v35, s26
	v_bfe_u32 v37, v51, 16, 1
	v_lshrrev_b32_e32 v35, 16, v35
	v_add3_u32 v37, v51, v37, s26
	v_and_or_b32 v39, v37, s27, v35
	v_bfe_u32 v35, v61, 16, 1
	v_add3_u32 v35, v61, v35, s26
	v_bfe_u32 v37, v63, 16, 1
	v_lshrrev_b32_e32 v35, 16, v35
	v_add3_u32 v37, v63, v37, s26
	v_and_or_b32 v40, v37, s27, v35
	v_bfe_u32 v35, v65, 16, 1
	v_add3_u32 v35, v65, v35, s26
	v_bfe_u32 v37, v67, 16, 1
	v_lshrrev_b32_e32 v35, 16, v35
	v_add3_u32 v37, v67, v37, s26
	v_lshlrev_b64 v[42:43], 11, v[42:43]
	v_and_or_b32 v41, v37, s27, v35
	ds_read2_b32 v[46:47], v55 offset0:16 offset1:24
	v_lshl_add_u64 v[42:43], v[44:45], 0, v[42:43]
	global_store_dwordx4 v[42:43], v[38:41], off
	ds_read2_b32 v[42:43], v55 offset0:49 offset1:57
	ds_read2_b32 v[48:49], v55 offset0:82 offset1:90
	ds_read2_b32 v[50:51], v55 offset0:115 offset1:123
	s_waitcnt lgkmcnt(3)
	v_bfe_u32 v35, v46, 16, 1
	v_add3_u32 v35, v46, v35, s26
	s_waitcnt lgkmcnt(2)
	v_bfe_u32 v37, v42, 16, 1
	ds_read2_b32 v[60:61], v55 offset0:148 offset1:156
	v_lshrrev_b32_e32 v35, 16, v35
	v_add3_u32 v37, v42, v37, s26
	ds_read2_b32 v[62:63], v55 offset0:181 offset1:189
	v_and_or_b32 v38, v37, s27, v35
	s_waitcnt lgkmcnt(3)
	v_bfe_u32 v35, v48, 16, 1
	v_add3_u32 v35, v48, v35, s26
	s_waitcnt lgkmcnt(2)
	v_bfe_u32 v37, v50, 16, 1
	ds_read2_b32 v[64:65], v55 offset0:214 offset1:222
	v_lshrrev_b32_e32 v35, 16, v35
	v_add3_u32 v37, v50, v37, s26
	ds_read2_b32 v[66:67], v55 offset0:247 offset1:255
	v_and_or_b32 v39, v37, s27, v35
	s_waitcnt lgkmcnt(3)
	v_bfe_u32 v35, v60, 16, 1
	v_add3_u32 v35, v60, v35, s26
	s_waitcnt lgkmcnt(2)
	v_bfe_u32 v37, v62, 16, 1
	v_lshrrev_b32_e32 v35, 16, v35
	v_add3_u32 v37, v62, v37, s26
	v_and_or_b32 v40, v37, s27, v35
	s_waitcnt lgkmcnt(1)
	v_bfe_u32 v35, v64, 16, 1
	v_add3_u32 v35, v64, v35, s26
	s_waitcnt lgkmcnt(0)
	v_bfe_u32 v37, v66, 16, 1
	v_lshrrev_b32_e32 v35, 16, v35
	v_add3_u32 v37, v66, v37, s26
	v_add_u32_e32 v68, s12, v57
	v_and_or_b32 v41, v37, s27, v35
	v_ashrrev_i32_e32 v69, 31, v68
	v_bfe_u32 v35, v47, 16, 1
	v_lshlrev_b64 v[68:69], 11, v[68:69]
	v_add3_u32 v35, v47, v35, s26
	v_bfe_u32 v37, v43, 16, 1
	v_lshl_add_u64 v[68:69], v[44:45], 0, v[68:69]
	v_lshrrev_b32_e32 v35, 16, v35
	v_add3_u32 v37, v43, v37, s26
	global_store_dwordx4 v[68:69], v[38:41], off
	v_add_u32_e32 v42, s12, v58
	v_ashrrev_i32_e32 v43, 31, v42
	v_and_or_b32 v38, v37, s27, v35
	v_bfe_u32 v35, v49, 16, 1
	v_add3_u32 v35, v49, v35, s26
	v_bfe_u32 v37, v51, 16, 1
	v_lshrrev_b32_e32 v35, 16, v35
	v_add3_u32 v37, v51, v37, s26
	v_and_or_b32 v39, v37, s27, v35
	v_bfe_u32 v35, v61, 16, 1
	v_add3_u32 v35, v61, v35, s26
	v_bfe_u32 v37, v63, 16, 1
	v_lshrrev_b32_e32 v35, 16, v35
	v_add3_u32 v37, v63, v37, s26
	v_and_or_b32 v40, v37, s27, v35
	v_bfe_u32 v35, v65, 16, 1
	v_add3_u32 v35, v65, v35, s26
	v_bfe_u32 v37, v67, 16, 1
	v_lshrrev_b32_e32 v35, 16, v35
	v_add3_u32 v37, v67, v37, s26
	v_lshlrev_b64 v[42:43], 11, v[42:43]
	v_and_or_b32 v41, v37, s27, v35
	v_lshl_add_u64 v[42:43], v[44:45], 0, v[42:43]
	global_store_dwordx4 v[42:43], v[38:41], off
	s_waitcnt lgkmcnt(0)

.LBB0_36:
	s_lshl_b32 s16, s14, 1
	s_lshl_b32 s17, s2, 1
	v_add_u32_e32 v62, s16, v40
	v_add_u32_e32 v60, s17, v35
	v_add_u32_e32 v64, s17, v37
	v_add_u32_e32 v66, s16, v42
	v_add_u32_e32 v68, s17, v41
	v_add_u32_e32 v70, s16, v44
	v_add_u32_e32 v72, s17, v43
	v_add_u32_e32 v74, s16, v46
	v_add_u32_e32 v76, s17, v45
	v_add_u32_e32 v78, s16, v48
	v_add_u32_e32 v80, s17, v47
	v_add_u32_e32 v82, s16, v50
	v_add_u32_e32 v84, s17, v49
	v_add_u32_e32 v86, s16, v52
	v_add_u32_e32 v88, s17, v51
	v_add_u32_e32 v90, s16, v54
	v_ashrrev_i32_e32 v63, 31, v62
	v_ashrrev_i32_e32 v61, 31, v60
	v_ashrrev_i32_e32 v67, 31, v66
	v_ashrrev_i32_e32 v65, 31, v64
	v_ashrrev_i32_e32 v71, 31, v70
	v_ashrrev_i32_e32 v69, 31, v68
	v_ashrrev_i32_e32 v75, 31, v74
	v_ashrrev_i32_e32 v73, 31, v72
	v_ashrrev_i32_e32 v79, 31, v78
	v_ashrrev_i32_e32 v77, 31, v76
	v_ashrrev_i32_e32 v83, 31, v82
	v_ashrrev_i32_e32 v81, 31, v80
	v_ashrrev_i32_e32 v87, 31, v86
	v_ashrrev_i32_e32 v85, 31, v84
	v_ashrrev_i32_e32 v91, 31, v90
	v_ashrrev_i32_e32 v89, 31, v88
	v_lshlrev_b64 v[62:63], 13, v[62:63]
	v_lshlrev_b64 v[60:61], 13, v[60:61]
	v_lshlrev_b64 v[64:65], 13, v[64:65]
	v_lshlrev_b64 v[66:67], 13, v[66:67]
	v_lshlrev_b64 v[68:69], 13, v[68:69]
	v_lshlrev_b64 v[70:71], 13, v[70:71]
	v_lshlrev_b64 v[72:73], 13, v[72:73]
	v_lshlrev_b64 v[74:75], 13, v[74:75]
	v_lshlrev_b64 v[76:77], 13, v[76:77]
	v_lshlrev_b64 v[78:79], 13, v[78:79]
	v_lshlrev_b64 v[80:81], 13, v[80:81]
	v_lshlrev_b64 v[82:83], 13, v[82:83]
	v_lshlrev_b64 v[84:85], 13, v[84:85]
	v_lshlrev_b64 v[86:87], 13, v[86:87]
	v_lshlrev_b64 v[88:89], 13, v[88:89]
	v_lshlrev_b64 v[90:91], 13, v[90:91]
	v_lshl_add_u64 v[62:63], v[38:39], 0, v[62:63]
	v_lshl_add_u64 v[60:61], v[38:39], 0, v[60:61]
	v_lshl_add_u64 v[66:67], v[38:39], 0, v[66:67]
	v_lshl_add_u64 v[64:65], v[38:39], 0, v[64:65]
	v_lshl_add_u64 v[70:71], v[38:39], 0, v[70:71]
	v_lshl_add_u64 v[68:69], v[38:39], 0, v[68:69]
	v_lshl_add_u64 v[74:75], v[38:39], 0, v[74:75]
	v_lshl_add_u64 v[72:73], v[38:39], 0, v[72:73]
	v_lshl_add_u64 v[78:79], v[38:39], 0, v[78:79]
	v_lshl_add_u64 v[76:77], v[38:39], 0, v[76:77]
	v_lshl_add_u64 v[82:83], v[38:39], 0, v[82:83]
	v_lshl_add_u64 v[80:81], v[38:39], 0, v[80:81]
	v_lshl_add_u64 v[86:87], v[38:39], 0, v[86:87]
	v_lshl_add_u64 v[84:85], v[38:39], 0, v[84:85]
	v_lshl_add_u64 v[90:91], v[38:39], 0, v[90:91]
	v_lshl_add_u64 v[88:89], v[38:39], 0, v[88:89]
	global_load_dword v59, v[62:63], off
	global_load_dword v92, v[60:61], off
	global_load_dword v93, v[66:67], off
	global_load_dword v94, v[64:65], off
	global_load_dword v95, v[70:71], off
	global_load_dword v96, v[68:69], off
	global_load_dword v97, v[74:75], off
	global_load_dword v98, v[72:73], off
	global_load_dword v99, v[78:79], off
	global_load_dword v100, v[76:77], off
	global_load_dword v101, v[82:83], off
	global_load_dword v102, v[80:81], off
	global_load_dword v103, v[86:87], off
	global_load_dword v104, v[84:85], off
	global_load_dword v105, v[90:91], off
	global_load_dword v106, v[88:89], off
	s_add_i32 s14, s14, 16
	s_add_i32 s2, s2, 16
	s_add_i32 s15, s15, -16
	s_lshl_b32 s40, s14, 1
	s_lshl_b32 s41, s2, 1
	v_add_u32_e32 v162, s40, v40
	v_add_u32_e32 v160, s41, v35
	v_add_u32_e32 v164, s41, v37
	v_add_u32_e32 v166, s40, v42
	v_add_u32_e32 v168, s41, v41
	v_add_u32_e32 v170, s40, v44
	v_add_u32_e32 v172, s41, v43
	v_add_u32_e32 v174, s40, v46
	v_add_u32_e32 v176, s41, v45
	v_add_u32_e32 v178, s40, v48
	v_add_u32_e32 v180, s41, v47
	v_add_u32_e32 v182, s40, v50
	v_add_u32_e32 v184, s41, v49
	v_add_u32_e32 v186, s40, v52
	v_add_u32_e32 v188, s41, v51
	v_add_u32_e32 v190, s40, v54
	v_ashrrev_i32_e32 v163, 31, v162
	v_ashrrev_i32_e32 v161, 31, v160
	v_ashrrev_i32_e32 v167, 31, v166
	v_ashrrev_i32_e32 v165, 31, v164
	v_ashrrev_i32_e32 v171, 31, v170
	v_ashrrev_i32_e32 v169, 31, v168
	v_ashrrev_i32_e32 v175, 31, v174
	v_ashrrev_i32_e32 v173, 31, v172
	v_ashrrev_i32_e32 v179, 31, v178
	v_ashrrev_i32_e32 v177, 31, v176
	v_ashrrev_i32_e32 v183, 31, v182
	v_ashrrev_i32_e32 v181, 31, v180
	v_ashrrev_i32_e32 v187, 31, v186
	v_ashrrev_i32_e32 v185, 31, v184
	v_ashrrev_i32_e32 v191, 31, v190
	v_ashrrev_i32_e32 v189, 31, v188
	v_lshlrev_b64 v[162:163], 13, v[162:163]
	v_lshlrev_b64 v[160:161], 13, v[160:161]
	v_lshlrev_b64 v[164:165], 13, v[164:165]
	v_lshlrev_b64 v[166:167], 13, v[166:167]
	v_lshlrev_b64 v[168:169], 13, v[168:169]
	v_lshlrev_b64 v[170:171], 13, v[170:171]
	v_lshlrev_b64 v[172:173], 13, v[172:173]
	v_lshlrev_b64 v[174:175], 13, v[174:175]
	v_lshlrev_b64 v[176:177], 13, v[176:177]
	v_lshlrev_b64 v[178:179], 13, v[178:179]
	v_lshlrev_b64 v[180:181], 13, v[180:181]
	v_lshlrev_b64 v[182:183], 13, v[182:183]
	v_lshlrev_b64 v[184:185], 13, v[184:185]
	v_lshlrev_b64 v[186:187], 13, v[186:187]
	v_lshlrev_b64 v[188:189], 13, v[188:189]
	v_lshlrev_b64 v[190:191], 13, v[190:191]
	v_lshl_add_u64 v[162:163], v[38:39], 0, v[162:163]
	v_lshl_add_u64 v[160:161], v[38:39], 0, v[160:161]
	v_lshl_add_u64 v[166:167], v[38:39], 0, v[166:167]
	v_lshl_add_u64 v[164:165], v[38:39], 0, v[164:165]
	v_lshl_add_u64 v[170:171], v[38:39], 0, v[170:171]
	v_lshl_add_u64 v[168:169], v[38:39], 0, v[168:169]
	v_lshl_add_u64 v[174:175], v[38:39], 0, v[174:175]
	v_lshl_add_u64 v[172:173], v[38:39], 0, v[172:173]
	v_lshl_add_u64 v[178:179], v[38:39], 0, v[178:179]
	v_lshl_add_u64 v[176:177], v[38:39], 0, v[176:177]
	v_lshl_add_u64 v[182:183], v[38:39], 0, v[182:183]
	v_lshl_add_u64 v[180:181], v[38:39], 0, v[180:181]
	v_lshl_add_u64 v[186:187], v[38:39], 0, v[186:187]
	v_lshl_add_u64 v[184:185], v[38:39], 0, v[184:185]
	v_lshl_add_u64 v[190:191], v[38:39], 0, v[190:191]
	v_lshl_add_u64 v[188:189], v[38:39], 0, v[188:189]
	global_load_dword v159, v[162:163], off
	global_load_dword v192, v[160:161], off
	global_load_dword v193, v[166:167], off
	global_load_dword v194, v[164:165], off
	global_load_dword v195, v[170:171], off
	global_load_dword v196, v[168:169], off
	global_load_dword v197, v[174:175], off
	global_load_dword v198, v[172:173], off
	global_load_dword v199, v[178:179], off
	global_load_dword v200, v[176:177], off
	global_load_dword v201, v[182:183], off
	global_load_dword v202, v[180:181], off
	global_load_dword v203, v[186:187], off
	global_load_dword v204, v[184:185], off
	global_load_dword v205, v[190:191], off
	global_load_dword v206, v[188:189], off
	s_add_i32 s14, s14, 16
	s_add_i32 s2, s2, 16
	s_add_i32 s15, s15, -16
	v_add_u32_e32 v60, s16, v0
	v_add_u32_e32 v62, s17, v1
	v_add_u32_e32 v66, s17, v21
	v_add_u32_e32 v64, s16, v22
	v_add_u32_e32 v70, s17, v23
	v_add_u32_e32 v68, s16, v24
	v_add_u32_e32 v74, s17, v25
	v_add_u32_e32 v72, s16, v26
	v_add_u32_e32 v78, s17, v27
	v_add_u32_e32 v76, s16, v28
	v_add_u32_e32 v82, s17, v29
	v_add_u32_e32 v80, s16, v30
	v_add_u32_e32 v86, s17, v31
	v_add_u32_e32 v84, s16, v32
	v_add_u32_e32 v90, s17, v33
	v_add_u32_e32 v88, s16, v34
	v_mad_u64_u32 v[60:61], s[16:17], v60, s24, v[20:21]
	v_mad_u64_u32 v[62:63], s[16:17], v62, s24, v[20:21]
	v_mad_u64_u32 v[64:65], s[16:17], v64, s24, v[20:21]
	v_mad_u64_u32 v[66:67], s[16:17], v66, s24, v[20:21]
	v_mad_u64_u32 v[68:69], s[16:17], v68, s24, v[20:21]
	v_mad_u64_u32 v[70:71], s[16:17], v70, s24, v[20:21]
	v_mad_u64_u32 v[72:73], s[16:17], v72, s24, v[20:21]
	v_mad_u64_u32 v[74:75], s[16:17], v74, s24, v[20:21]
	v_mad_u64_u32 v[76:77], s[16:17], v76, s24, v[20:21]
	v_mad_u64_u32 v[78:79], s[16:17], v78, s24, v[20:21]
	v_mad_u64_u32 v[80:81], s[16:17], v80, s24, v[20:21]
	v_mad_u64_u32 v[82:83], s[16:17], v82, s24, v[20:21]
	v_mad_u64_u32 v[84:85], s[16:17], v84, s24, v[20:21]
	v_mad_u64_u32 v[86:87], s[16:17], v86, s24, v[20:21]
	v_mad_u64_u32 v[88:89], s[16:17], v88, s24, v[20:21]
	v_mad_u64_u32 v[90:91], s[16:17], v90, s24, v[20:21]
	s_waitcnt vmcnt(31)
	ds_write_b32 v60, v59
	s_waitcnt vmcnt(30)
	ds_write_b32 v62, v92
	s_waitcnt vmcnt(29)
	ds_write_b32 v64, v93
	s_waitcnt vmcnt(28)
	ds_write_b32 v66, v94
	s_waitcnt vmcnt(27)
	ds_write_b32 v68, v95
	s_waitcnt vmcnt(26)
	ds_write_b32 v70, v96
	s_waitcnt vmcnt(25)
	ds_write_b32 v72, v97
	s_waitcnt vmcnt(24)
	ds_write_b32 v74, v98
	s_waitcnt vmcnt(23)
	ds_write_b32 v76, v99
	s_waitcnt vmcnt(22)
	ds_write_b32 v78, v100
	s_waitcnt vmcnt(21)
	ds_write_b32 v80, v101
	s_waitcnt vmcnt(20)
	ds_write_b32 v82, v102
	s_waitcnt vmcnt(19)
	ds_write_b32 v84, v103
	s_waitcnt vmcnt(18)
	ds_write_b32 v86, v104
	s_waitcnt vmcnt(17)
	ds_write_b32 v88, v105
	s_waitcnt vmcnt(16)
	ds_write_b32 v90, v106
	v_add_u32_e32 v160, s40, v0
	v_add_u32_e32 v162, s41, v1
	v_add_u32_e32 v166, s41, v21
	v_add_u32_e32 v164, s40, v22
	v_add_u32_e32 v170, s41, v23
	v_add_u32_e32 v168, s40, v24
	v_add_u32_e32 v174, s41, v25
	v_add_u32_e32 v172, s40, v26
	v_add_u32_e32 v178, s41, v27
	v_add_u32_e32 v176, s40, v28
	v_add_u32_e32 v182, s41, v29
	v_add_u32_e32 v180, s40, v30
	v_add_u32_e32 v186, s41, v31
	v_add_u32_e32 v184, s40, v32
	v_add_u32_e32 v190, s41, v33
	v_add_u32_e32 v188, s40, v34
	v_mad_u64_u32 v[160:161], s[40:41], v160, s24, v[20:21]
	v_mad_u64_u32 v[162:163], s[40:41], v162, s24, v[20:21]
	v_mad_u64_u32 v[164:165], s[40:41], v164, s24, v[20:21]
	v_mad_u64_u32 v[166:167], s[40:41], v166, s24, v[20:21]
	v_mad_u64_u32 v[168:169], s[40:41], v168, s24, v[20:21]
	v_mad_u64_u32 v[170:171], s[40:41], v170, s24, v[20:21]
	v_mad_u64_u32 v[172:173], s[40:41], v172, s24, v[20:21]
	v_mad_u64_u32 v[174:175], s[40:41], v174, s24, v[20:21]
	v_mad_u64_u32 v[176:177], s[40:41], v176, s24, v[20:21]
	v_mad_u64_u32 v[178:179], s[40:41], v178, s24, v[20:21]
	v_mad_u64_u32 v[180:181], s[40:41], v180, s24, v[20:21]
	v_mad_u64_u32 v[182:183], s[40:41], v182, s24, v[20:21]
	v_mad_u64_u32 v[184:185], s[40:41], v184, s24, v[20:21]
	v_mad_u64_u32 v[186:187], s[40:41], v186, s24, v[20:21]
	v_mad_u64_u32 v[188:189], s[40:41], v188, s24, v[20:21]
	v_mad_u64_u32 v[190:191], s[40:41], v190, s24, v[20:21]
	s_waitcnt vmcnt(15)
	ds_write_b32 v160, v159
	s_waitcnt vmcnt(14)
	ds_write_b32 v162, v192
	s_waitcnt vmcnt(13)
	ds_write_b32 v164, v193
	s_waitcnt vmcnt(12)
	ds_write_b32 v166, v194
	s_waitcnt vmcnt(11)
	ds_write_b32 v168, v195
	s_waitcnt vmcnt(10)
	ds_write_b32 v170, v196
	s_waitcnt vmcnt(9)
	ds_write_b32 v172, v197
	s_waitcnt vmcnt(8)
	ds_write_b32 v174, v198
	s_waitcnt vmcnt(7)
	ds_write_b32 v176, v199
	s_waitcnt vmcnt(6)
	ds_write_b32 v178, v200
	s_waitcnt vmcnt(5)
	ds_write_b32 v180, v201
	s_waitcnt vmcnt(4)
	ds_write_b32 v182, v202
	s_waitcnt vmcnt(3)
	ds_write_b32 v184, v203
	s_waitcnt vmcnt(2)
	ds_write_b32 v186, v204
	s_waitcnt vmcnt(1)
	ds_write_b32 v188, v205
	s_waitcnt vmcnt(0)
	ds_write_b32 v190, v206
	s_waitcnt lgkmcnt(0)
	ds_read2_b32 v[42:43], v55 offset1:8
	ds_read2_b32 v[46:47], v55 offset0:33 offset1:41
	ds_read2_b32 v[48:49], v55 offset0:66 offset1:74
	ds_read2_b32 v[50:51], v55 offset0:99 offset1:107
	ds_read2_b32 v[60:61], v55 offset0:132 offset1:140
	ds_read2_b32 v[62:63], v55 offset0:165 offset1:173
	s_waitcnt lgkmcnt(5)
	v_bfe_u32 v35, v42, 16, 1
	v_add3_u32 v35, v42, v35, s26
	s_waitcnt lgkmcnt(4)
	v_bfe_u32 v37, v46, 16, 1
	v_lshrrev_b32_e32 v35, 16, v35
	v_add3_u32 v37, v46, v37, s26
	v_and_or_b32 v38, v37, s27, v35
	s_waitcnt lgkmcnt(3)
	v_bfe_u32 v35, v48, 16, 1
	v_add3_u32 v35, v48, v35, s26
	s_waitcnt lgkmcnt(2)
	v_bfe_u32 v37, v50, 16, 1
	ds_read2_b32 v[64:65], v55 offset0:198 offset1:206
	v_lshrrev_b32_e32 v35, 16, v35
	v_add3_u32 v37, v50, v37, s26
	ds_read2_b32 v[66:67], v55 offset0:231 offset1:239
	v_and_or_b32 v39, v37, s27, v35
	s_waitcnt lgkmcnt(3)
	v_bfe_u32 v35, v60, 16, 1
	v_add3_u32 v35, v60, v35, s26
	s_waitcnt lgkmcnt(2)
	v_bfe_u32 v37, v62, 16, 1
	v_lshrrev_b32_e32 v35, 16, v35
	v_add3_u32 v37, v62, v37, s26
	v_and_or_b32 v40, v37, s27, v35
	s_waitcnt lgkmcnt(1)
	v_bfe_u32 v35, v64, 16, 1
	v_add3_u32 v35, v64, v35, s26
	s_waitcnt lgkmcnt(0)
	v_bfe_u32 v37, v66, 16, 1
	v_lshrrev_b32_e32 v35, 16, v35
	v_add3_u32 v37, v66, v37, s26
	v_add_u32_e32 v68, s12, v53
	s_lshl_b32 s2, s13, 1
	v_and_or_b32 v41, v37, s27, v35
	v_ashrrev_i32_e32 v69, 31, v68
	v_bfe_u32 v35, v43, 16, 1
	v_lshl_add_u64 v[44:45], v[10:11], 0, s[2:3]
	v_lshlrev_b64 v[68:69], 11, v[68:69]
	v_add3_u32 v35, v43, v35, s26
	v_bfe_u32 v37, v47, 16, 1
	v_lshl_add_u64 v[68:69], v[44:45], 0, v[68:69]
	v_lshrrev_b32_e32 v35, 16, v35
	v_add3_u32 v37, v47, v37, s26
	global_store_dwordx4 v[68:69], v[38:41], off
	v_add_u32_e32 v42, s12, v56
	v_ashrrev_i32_e32 v43, 31, v42
	v_and_or_b32 v38, v37, s27, v35
	v_bfe_u32 v35, v49, 16, 1
	v_add3_u32 v35, v49, v35, s26
	v_bfe_u32 v37, v51, 16, 1
	v_lshrrev_b32_e32 v35, 16, v35
	v_add3_u32 v37, v51, v37, s26
	v_and_or_b32 v39, v37, s27, v35
	v_bfe_u32 v35, v61, 16, 1
	v_add3_u32 v35, v61, v35, s26
	v_bfe_u32 v37, v63, 16, 1
	v_lshrrev_b32_e32 v35, 16, v35
	v_add3_u32 v37, v63, v37, s26
	v_and_or_b32 v40, v37, s27, v35
	v_bfe_u32 v35, v65, 16, 1
	v_add3_u32 v35, v65, v35, s26
	v_bfe_u32 v37, v67, 16, 1
	v_lshrrev_b32_e32 v35, 16, v35
	v_add3_u32 v37, v67, v37, s26
	v_lshlrev_b64 v[42:43], 11, v[42:43]
	v_and_or_b32 v41, v37, s27, v35
	ds_read2_b32 v[46:47], v55 offset0:16 offset1:24
	v_lshl_add_u64 v[42:43], v[44:45], 0, v[42:43]
	global_store_dwordx4 v[42:43], v[38:41], off
	ds_read2_b32 v[42:43], v55 offset0:49 offset1:57
	ds_read2_b32 v[48:49], v55 offset0:82 offset1:90
	ds_read2_b32 v[50:51], v55 offset0:115 offset1:123
	s_waitcnt lgkmcnt(3)
	v_bfe_u32 v35, v46, 16, 1
	v_add3_u32 v35, v46, v35, s26
	s_waitcnt lgkmcnt(2)
	v_bfe_u32 v37, v42, 16, 1
	ds_read2_b32 v[60:61], v55 offset0:148 offset1:156
	v_lshrrev_b32_e32 v35, 16, v35
	v_add3_u32 v37, v42, v37, s26
	ds_read2_b32 v[62:63], v55 offset0:181 offset1:189
	v_and_or_b32 v38, v37, s27, v35
	s_waitcnt lgkmcnt(3)
	v_bfe_u32 v35, v48, 16, 1
	v_add3_u32 v35, v48, v35, s26
	s_waitcnt lgkmcnt(2)
	v_bfe_u32 v37, v50, 16, 1
	ds_read2_b32 v[64:65], v55 offset0:214 offset1:222
	v_lshrrev_b32_e32 v35, 16, v35
	v_add3_u32 v37, v50, v37, s26
	ds_read2_b32 v[66:67], v55 offset0:247 offset1:255
	v_and_or_b32 v39, v37, s27, v35
	s_waitcnt lgkmcnt(3)
	v_bfe_u32 v35, v60, 16, 1
	v_add3_u32 v35, v60, v35, s26
	s_waitcnt lgkmcnt(2)
	v_bfe_u32 v37, v62, 16, 1
	v_lshrrev_b32_e32 v35, 16, v35
	v_add3_u32 v37, v62, v37, s26
	v_and_or_b32 v40, v37, s27, v35
	s_waitcnt lgkmcnt(1)
	v_bfe_u32 v35, v64, 16, 1
	v_add3_u32 v35, v64, v35, s26
	s_waitcnt lgkmcnt(0)
	v_bfe_u32 v37, v66, 16, 1
	v_lshrrev_b32_e32 v35, 16, v35
	v_add3_u32 v37, v66, v37, s26
	v_add_u32_e32 v68, s12, v57
	v_and_or_b32 v41, v37, s27, v35
	v_ashrrev_i32_e32 v69, 31, v68
	v_bfe_u32 v35, v47, 16, 1
	v_lshlrev_b64 v[68:69], 11, v[68:69]
	v_add3_u32 v35, v47, v35, s26
	v_bfe_u32 v37, v43, 16, 1
	v_lshl_add_u64 v[68:69], v[44:45], 0, v[68:69]
	v_lshrrev_b32_e32 v35, 16, v35
	v_add3_u32 v37, v43, v37, s26
	global_store_dwordx4 v[68:69], v[38:41], off
	v_add_u32_e32 v42, s12, v58
	v_ashrrev_i32_e32 v43, 31, v42
	v_and_or_b32 v38, v37, s27, v35
	v_bfe_u32 v35, v49, 16, 1
	v_add3_u32 v35, v49, v35, s26
	v_bfe_u32 v37, v51, 16, 1
	v_lshrrev_b32_e32 v35, 16, v35
	v_add3_u32 v37, v51, v37, s26
	v_and_or_b32 v39, v37, s27, v35
	v_bfe_u32 v35, v61, 16, 1
	v_add3_u32 v35, v61, v35, s26
	v_bfe_u32 v37, v63, 16, 1
	v_lshrrev_b32_e32 v35, 16, v35
	v_add3_u32 v37, v63, v37, s26
	v_and_or_b32 v40, v37, s27, v35
	v_bfe_u32 v35, v65, 16, 1
	v_add3_u32 v35, v65, v35, s26
	v_bfe_u32 v37, v67, 16, 1
	v_lshrrev_b32_e32 v35, 16, v35
	v_add3_u32 v37, v67, v37, s26
	v_lshlrev_b64 v[42:43], 11, v[42:43]
	v_and_or_b32 v41, v37, s27, v35
	v_lshl_add_u64 v[42:43], v[44:45], 0, v[42:43]
	global_store_dwordx4 v[42:43], v[38:41], off
	s_waitcnt lgkmcnt(0)

.LBB0_41:
	s_lshl_b32 s16, s2, 1
	s_lshl_b32 s17, s14, 1
	v_add_u32_e32 v62, s16, v40
	v_add_u32_e32 v60, s17, v35
	v_add_u32_e32 v64, s17, v37
	v_add_u32_e32 v66, s16, v42
	v_add_u32_e32 v68, s17, v41
	v_add_u32_e32 v70, s16, v44
	v_add_u32_e32 v72, s17, v43
	v_add_u32_e32 v74, s16, v46
	v_add_u32_e32 v76, s17, v45
	v_add_u32_e32 v78, s16, v48
	v_add_u32_e32 v80, s17, v47
	v_add_u32_e32 v82, s16, v50
	v_add_u32_e32 v84, s17, v49
	v_add_u32_e32 v86, s16, v52
	v_add_u32_e32 v88, s17, v51
	v_add_u32_e32 v90, s16, v54
	v_ashrrev_i32_e32 v63, 31, v62
	v_ashrrev_i32_e32 v61, 31, v60
	v_ashrrev_i32_e32 v67, 31, v66
	v_ashrrev_i32_e32 v65, 31, v64
	v_ashrrev_i32_e32 v71, 31, v70
	v_ashrrev_i32_e32 v69, 31, v68
	v_ashrrev_i32_e32 v75, 31, v74
	v_ashrrev_i32_e32 v73, 31, v72
	v_ashrrev_i32_e32 v79, 31, v78
	v_ashrrev_i32_e32 v77, 31, v76
	v_ashrrev_i32_e32 v83, 31, v82
	v_ashrrev_i32_e32 v81, 31, v80
	v_ashrrev_i32_e32 v87, 31, v86
	v_ashrrev_i32_e32 v85, 31, v84
	v_ashrrev_i32_e32 v91, 31, v90
	v_ashrrev_i32_e32 v89, 31, v88
	v_lshlrev_b64 v[62:63], 12, v[62:63]
	v_lshlrev_b64 v[60:61], 12, v[60:61]
	v_lshlrev_b64 v[64:65], 12, v[64:65]
	v_lshlrev_b64 v[66:67], 12, v[66:67]
	v_lshlrev_b64 v[68:69], 12, v[68:69]
	v_lshlrev_b64 v[70:71], 12, v[70:71]
	v_lshlrev_b64 v[72:73], 12, v[72:73]
	v_lshlrev_b64 v[74:75], 12, v[74:75]
	v_lshlrev_b64 v[76:77], 12, v[76:77]
	v_lshlrev_b64 v[78:79], 12, v[78:79]
	v_lshlrev_b64 v[80:81], 12, v[80:81]
	v_lshlrev_b64 v[82:83], 12, v[82:83]
	v_lshlrev_b64 v[84:85], 12, v[84:85]
	v_lshlrev_b64 v[86:87], 12, v[86:87]
	v_lshlrev_b64 v[88:89], 12, v[88:89]
	v_lshlrev_b64 v[90:91], 12, v[90:91]
	v_lshl_add_u64 v[62:63], v[38:39], 0, v[62:63]
	v_lshl_add_u64 v[60:61], v[38:39], 0, v[60:61]
	v_lshl_add_u64 v[66:67], v[38:39], 0, v[66:67]
	v_lshl_add_u64 v[64:65], v[38:39], 0, v[64:65]
	v_lshl_add_u64 v[70:71], v[38:39], 0, v[70:71]
	v_lshl_add_u64 v[68:69], v[38:39], 0, v[68:69]
	v_lshl_add_u64 v[74:75], v[38:39], 0, v[74:75]
	v_lshl_add_u64 v[72:73], v[38:39], 0, v[72:73]
	v_lshl_add_u64 v[78:79], v[38:39], 0, v[78:79]
	v_lshl_add_u64 v[76:77], v[38:39], 0, v[76:77]
	v_lshl_add_u64 v[82:83], v[38:39], 0, v[82:83]
	v_lshl_add_u64 v[80:81], v[38:39], 0, v[80:81]
	v_lshl_add_u64 v[86:87], v[38:39], 0, v[86:87]
	v_lshl_add_u64 v[84:85], v[38:39], 0, v[84:85]
	v_lshl_add_u64 v[90:91], v[38:39], 0, v[90:91]
	v_lshl_add_u64 v[88:89], v[38:39], 0, v[88:89]
	global_load_dword v59, v[62:63], off
	global_load_dword v92, v[60:61], off
	global_load_dword v93, v[66:67], off
	global_load_dword v94, v[64:65], off
	global_load_dword v95, v[70:71], off
	global_load_dword v96, v[68:69], off
	global_load_dword v97, v[74:75], off
	global_load_dword v98, v[72:73], off
	global_load_dword v99, v[78:79], off
	global_load_dword v100, v[76:77], off
	global_load_dword v101, v[82:83], off
	global_load_dword v102, v[80:81], off
	global_load_dword v103, v[86:87], off
	global_load_dword v104, v[84:85], off
	global_load_dword v105, v[90:91], off
	global_load_dword v106, v[88:89], off
	s_add_i32 s2, s2, 16
	s_add_i32 s14, s14, 16
	s_add_i32 s15, s15, -16
	s_lshl_b32 s40, s2, 1
	s_lshl_b32 s41, s14, 1
	v_add_u32_e32 v162, s40, v40
	v_add_u32_e32 v160, s41, v35
	v_add_u32_e32 v164, s41, v37
	v_add_u32_e32 v166, s40, v42
	v_add_u32_e32 v168, s41, v41
	v_add_u32_e32 v170, s40, v44
	v_add_u32_e32 v172, s41, v43
	v_add_u32_e32 v174, s40, v46
	v_add_u32_e32 v176, s41, v45
	v_add_u32_e32 v178, s40, v48
	v_add_u32_e32 v180, s41, v47
	v_add_u32_e32 v182, s40, v50
	v_add_u32_e32 v184, s41, v49
	v_add_u32_e32 v186, s40, v52
	v_add_u32_e32 v188, s41, v51
	v_add_u32_e32 v190, s40, v54
	v_ashrrev_i32_e32 v163, 31, v162
	v_ashrrev_i32_e32 v161, 31, v160
	v_ashrrev_i32_e32 v167, 31, v166
	v_ashrrev_i32_e32 v165, 31, v164
	v_ashrrev_i32_e32 v171, 31, v170
	v_ashrrev_i32_e32 v169, 31, v168
	v_ashrrev_i32_e32 v175, 31, v174
	v_ashrrev_i32_e32 v173, 31, v172
	v_ashrrev_i32_e32 v179, 31, v178
	v_ashrrev_i32_e32 v177, 31, v176
	v_ashrrev_i32_e32 v183, 31, v182
	v_ashrrev_i32_e32 v181, 31, v180
	v_ashrrev_i32_e32 v187, 31, v186
	v_ashrrev_i32_e32 v185, 31, v184
	v_ashrrev_i32_e32 v191, 31, v190
	v_ashrrev_i32_e32 v189, 31, v188
	v_lshlrev_b64 v[162:163], 12, v[162:163]
	v_lshlrev_b64 v[160:161], 12, v[160:161]
	v_lshlrev_b64 v[164:165], 12, v[164:165]
	v_lshlrev_b64 v[166:167], 12, v[166:167]
	v_lshlrev_b64 v[168:169], 12, v[168:169]
	v_lshlrev_b64 v[170:171], 12, v[170:171]
	v_lshlrev_b64 v[172:173], 12, v[172:173]
	v_lshlrev_b64 v[174:175], 12, v[174:175]
	v_lshlrev_b64 v[176:177], 12, v[176:177]
	v_lshlrev_b64 v[178:179], 12, v[178:179]
	v_lshlrev_b64 v[180:181], 12, v[180:181]
	v_lshlrev_b64 v[182:183], 12, v[182:183]
	v_lshlrev_b64 v[184:185], 12, v[184:185]
	v_lshlrev_b64 v[186:187], 12, v[186:187]
	v_lshlrev_b64 v[188:189], 12, v[188:189]
	v_lshlrev_b64 v[190:191], 12, v[190:191]
	v_lshl_add_u64 v[162:163], v[38:39], 0, v[162:163]
	v_lshl_add_u64 v[160:161], v[38:39], 0, v[160:161]
	v_lshl_add_u64 v[166:167], v[38:39], 0, v[166:167]
	v_lshl_add_u64 v[164:165], v[38:39], 0, v[164:165]
	v_lshl_add_u64 v[170:171], v[38:39], 0, v[170:171]
	v_lshl_add_u64 v[168:169], v[38:39], 0, v[168:169]
	v_lshl_add_u64 v[174:175], v[38:39], 0, v[174:175]
	v_lshl_add_u64 v[172:173], v[38:39], 0, v[172:173]
	v_lshl_add_u64 v[178:179], v[38:39], 0, v[178:179]
	v_lshl_add_u64 v[176:177], v[38:39], 0, v[176:177]
	v_lshl_add_u64 v[182:183], v[38:39], 0, v[182:183]
	v_lshl_add_u64 v[180:181], v[38:39], 0, v[180:181]
	v_lshl_add_u64 v[186:187], v[38:39], 0, v[186:187]
	v_lshl_add_u64 v[184:185], v[38:39], 0, v[184:185]
	v_lshl_add_u64 v[190:191], v[38:39], 0, v[190:191]
	v_lshl_add_u64 v[188:189], v[38:39], 0, v[188:189]
	global_load_dword v159, v[162:163], off
	global_load_dword v192, v[160:161], off
	global_load_dword v193, v[166:167], off
	global_load_dword v194, v[164:165], off
	global_load_dword v195, v[170:171], off
	global_load_dword v196, v[168:169], off
	global_load_dword v197, v[174:175], off
	global_load_dword v198, v[172:173], off
	global_load_dword v199, v[178:179], off
	global_load_dword v200, v[176:177], off
	global_load_dword v201, v[182:183], off
	global_load_dword v202, v[180:181], off
	global_load_dword v203, v[186:187], off
	global_load_dword v204, v[184:185], off
	global_load_dword v205, v[190:191], off
	global_load_dword v206, v[188:189], off
	s_add_i32 s2, s2, 16
	s_add_i32 s14, s14, 16
	s_add_i32 s15, s15, -16
	v_add_u32_e32 v60, s16, v0
	v_add_u32_e32 v62, s17, v1
	v_add_u32_e32 v66, s17, v21
	v_add_u32_e32 v64, s16, v22
	v_add_u32_e32 v70, s17, v23
	v_add_u32_e32 v68, s16, v24
	v_add_u32_e32 v74, s17, v25
	v_add_u32_e32 v72, s16, v26
	v_add_u32_e32 v78, s17, v27
	v_add_u32_e32 v76, s16, v28
	v_add_u32_e32 v82, s17, v29
	v_add_u32_e32 v80, s16, v30
	v_add_u32_e32 v86, s17, v31
	v_add_u32_e32 v84, s16, v32
	v_add_u32_e32 v90, s17, v33
	v_add_u32_e32 v88, s16, v34
	v_mad_u64_u32 v[60:61], s[16:17], v60, s24, v[20:21]
	v_mad_u64_u32 v[62:63], s[16:17], v62, s24, v[20:21]
	v_mad_u64_u32 v[64:65], s[16:17], v64, s24, v[20:21]
	v_mad_u64_u32 v[66:67], s[16:17], v66, s24, v[20:21]
	v_mad_u64_u32 v[68:69], s[16:17], v68, s24, v[20:21]
	v_mad_u64_u32 v[70:71], s[16:17], v70, s24, v[20:21]
	v_mad_u64_u32 v[72:73], s[16:17], v72, s24, v[20:21]
	v_mad_u64_u32 v[74:75], s[16:17], v74, s24, v[20:21]
	v_mad_u64_u32 v[76:77], s[16:17], v76, s24, v[20:21]
	v_mad_u64_u32 v[78:79], s[16:17], v78, s24, v[20:21]
	v_mad_u64_u32 v[80:81], s[16:17], v80, s24, v[20:21]
	v_mad_u64_u32 v[82:83], s[16:17], v82, s24, v[20:21]
	v_mad_u64_u32 v[84:85], s[16:17], v84, s24, v[20:21]
	v_mad_u64_u32 v[86:87], s[16:17], v86, s24, v[20:21]
	v_mad_u64_u32 v[88:89], s[16:17], v88, s24, v[20:21]
	v_mad_u64_u32 v[90:91], s[16:17], v90, s24, v[20:21]
	s_waitcnt vmcnt(31)
	ds_write_b32 v60, v59
	s_waitcnt vmcnt(30)
	ds_write_b32 v62, v92
	s_waitcnt vmcnt(29)
	ds_write_b32 v64, v93
	s_waitcnt vmcnt(28)
	ds_write_b32 v66, v94
	s_waitcnt vmcnt(27)
	ds_write_b32 v68, v95
	s_waitcnt vmcnt(26)
	ds_write_b32 v70, v96
	s_waitcnt vmcnt(25)
	ds_write_b32 v72, v97
	s_waitcnt vmcnt(24)
	ds_write_b32 v74, v98
	s_waitcnt vmcnt(23)
	ds_write_b32 v76, v99
	s_waitcnt vmcnt(22)
	ds_write_b32 v78, v100
	s_waitcnt vmcnt(21)
	ds_write_b32 v80, v101
	s_waitcnt vmcnt(20)
	ds_write_b32 v82, v102
	s_waitcnt vmcnt(19)
	ds_write_b32 v84, v103
	s_waitcnt vmcnt(18)
	ds_write_b32 v86, v104
	s_waitcnt vmcnt(17)
	ds_write_b32 v88, v105
	s_waitcnt vmcnt(16)
	ds_write_b32 v90, v106
	v_add_u32_e32 v160, s40, v0
	v_add_u32_e32 v162, s41, v1
	v_add_u32_e32 v166, s41, v21
	v_add_u32_e32 v164, s40, v22
	v_add_u32_e32 v170, s41, v23
	v_add_u32_e32 v168, s40, v24
	v_add_u32_e32 v174, s41, v25
	v_add_u32_e32 v172, s40, v26
	v_add_u32_e32 v178, s41, v27
	v_add_u32_e32 v176, s40, v28
	v_add_u32_e32 v182, s41, v29
	v_add_u32_e32 v180, s40, v30
	v_add_u32_e32 v186, s41, v31
	v_add_u32_e32 v184, s40, v32
	v_add_u32_e32 v190, s41, v33
	v_add_u32_e32 v188, s40, v34
	v_mad_u64_u32 v[160:161], s[40:41], v160, s24, v[20:21]
	v_mad_u64_u32 v[162:163], s[40:41], v162, s24, v[20:21]
	v_mad_u64_u32 v[164:165], s[40:41], v164, s24, v[20:21]
	v_mad_u64_u32 v[166:167], s[40:41], v166, s24, v[20:21]
	v_mad_u64_u32 v[168:169], s[40:41], v168, s24, v[20:21]
	v_mad_u64_u32 v[170:171], s[40:41], v170, s24, v[20:21]
	v_mad_u64_u32 v[172:173], s[40:41], v172, s24, v[20:21]
	v_mad_u64_u32 v[174:175], s[40:41], v174, s24, v[20:21]
	v_mad_u64_u32 v[176:177], s[40:41], v176, s24, v[20:21]
	v_mad_u64_u32 v[178:179], s[40:41], v178, s24, v[20:21]
	v_mad_u64_u32 v[180:181], s[40:41], v180, s24, v[20:21]
	v_mad_u64_u32 v[182:183], s[40:41], v182, s24, v[20:21]
	v_mad_u64_u32 v[184:185], s[40:41], v184, s24, v[20:21]
	v_mad_u64_u32 v[186:187], s[40:41], v186, s24, v[20:21]
	v_mad_u64_u32 v[188:189], s[40:41], v188, s24, v[20:21]
	v_mad_u64_u32 v[190:191], s[40:41], v190, s24, v[20:21]
	s_waitcnt vmcnt(15)
	ds_write_b32 v160, v159
	s_waitcnt vmcnt(14)
	ds_write_b32 v162, v192
	s_waitcnt vmcnt(13)
	ds_write_b32 v164, v193
	s_waitcnt vmcnt(12)
	ds_write_b32 v166, v194
	s_waitcnt vmcnt(11)
	ds_write_b32 v168, v195
	s_waitcnt vmcnt(10)
	ds_write_b32 v170, v196
	s_waitcnt vmcnt(9)
	ds_write_b32 v172, v197
	s_waitcnt vmcnt(8)
	ds_write_b32 v174, v198
	s_waitcnt vmcnt(7)
	ds_write_b32 v176, v199
	s_waitcnt vmcnt(6)
	ds_write_b32 v178, v200
	s_waitcnt vmcnt(5)
	ds_write_b32 v180, v201
	s_waitcnt vmcnt(4)
	ds_write_b32 v182, v202
	s_waitcnt vmcnt(3)
	ds_write_b32 v184, v203
	s_waitcnt vmcnt(2)
	ds_write_b32 v186, v204
	s_waitcnt vmcnt(1)
	ds_write_b32 v188, v205
	s_waitcnt vmcnt(0)
	ds_write_b32 v190, v206
	s_waitcnt lgkmcnt(0)
	ds_read2_b32 v[42:43], v55 offset1:8
	ds_read2_b32 v[46:47], v55 offset0:33 offset1:41
	ds_read2_b32 v[48:49], v55 offset0:66 offset1:74
	ds_read2_b32 v[50:51], v55 offset0:99 offset1:107
	ds_read2_b32 v[60:61], v55 offset0:132 offset1:140
	ds_read2_b32 v[62:63], v55 offset0:165 offset1:173
	s_waitcnt lgkmcnt(5)
	v_bfe_u32 v35, v42, 16, 1
	v_add3_u32 v35, v42, v35, s26
	s_waitcnt lgkmcnt(4)
	v_bfe_u32 v37, v46, 16, 1
	v_lshrrev_b32_e32 v35, 16, v35
	v_add3_u32 v37, v46, v37, s26
	v_and_or_b32 v38, v37, s27, v35
	s_waitcnt lgkmcnt(3)
	v_bfe_u32 v35, v48, 16, 1
	v_add3_u32 v35, v48, v35, s26
	s_waitcnt lgkmcnt(2)
	v_bfe_u32 v37, v50, 16, 1
	ds_read2_b32 v[64:65], v55 offset0:198 offset1:206
	v_lshrrev_b32_e32 v35, 16, v35
	v_add3_u32 v37, v50, v37, s26
	ds_read2_b32 v[66:67], v55 offset0:231 offset1:239
	v_and_or_b32 v39, v37, s27, v35
	s_waitcnt lgkmcnt(3)
	v_bfe_u32 v35, v60, 16, 1
	v_add3_u32 v35, v60, v35, s26
	s_waitcnt lgkmcnt(2)
	v_bfe_u32 v37, v62, 16, 1
	v_lshrrev_b32_e32 v35, 16, v35
	v_add3_u32 v37, v62, v37, s26
	v_and_or_b32 v40, v37, s27, v35
	s_waitcnt lgkmcnt(1)
	v_bfe_u32 v35, v64, 16, 1
	v_add3_u32 v35, v64, v35, s26
	s_waitcnt lgkmcnt(0)
	v_bfe_u32 v37, v66, 16, 1
	v_lshrrev_b32_e32 v35, 16, v35
	v_add3_u32 v37, v66, v37, s26
	v_add_u32_e32 v68, s12, v53
	s_lshl_b32 s2, s13, 1
	v_and_or_b32 v41, v37, s27, v35
	v_ashrrev_i32_e32 v69, 31, v68
	v_bfe_u32 v35, v43, 16, 1
	v_lshl_add_u64 v[44:45], v[14:15], 0, s[2:3]
	v_lshlrev_b64 v[68:69], 11, v[68:69]
	v_add3_u32 v35, v43, v35, s26
	v_bfe_u32 v37, v47, 16, 1
	v_lshl_add_u64 v[68:69], v[44:45], 0, v[68:69]
	v_lshrrev_b32_e32 v35, 16, v35
	v_add3_u32 v37, v47, v37, s26
	global_store_dwordx4 v[68:69], v[38:41], off
	v_add_u32_e32 v42, s12, v56
	v_ashrrev_i32_e32 v43, 31, v42
	v_and_or_b32 v38, v37, s27, v35
	v_bfe_u32 v35, v49, 16, 1
	v_add3_u32 v35, v49, v35, s26
	v_bfe_u32 v37, v51, 16, 1
	v_lshrrev_b32_e32 v35, 16, v35
	v_add3_u32 v37, v51, v37, s26
	v_and_or_b32 v39, v37, s27, v35
	v_bfe_u32 v35, v61, 16, 1
	v_add3_u32 v35, v61, v35, s26
	v_bfe_u32 v37, v63, 16, 1
	v_lshrrev_b32_e32 v35, 16, v35
	v_add3_u32 v37, v63, v37, s26
	v_and_or_b32 v40, v37, s27, v35
	v_bfe_u32 v35, v65, 16, 1
	v_add3_u32 v35, v65, v35, s26
	v_bfe_u32 v37, v67, 16, 1
	v_lshrrev_b32_e32 v35, 16, v35
	v_add3_u32 v37, v67, v37, s26
	v_lshlrev_b64 v[42:43], 11, v[42:43]
	v_and_or_b32 v41, v37, s27, v35
	ds_read2_b32 v[46:47], v55 offset0:16 offset1:24
	v_lshl_add_u64 v[42:43], v[44:45], 0, v[42:43]
	global_store_dwordx4 v[42:43], v[38:41], off
	ds_read2_b32 v[42:43], v55 offset0:49 offset1:57
	ds_read2_b32 v[48:49], v55 offset0:82 offset1:90
	ds_read2_b32 v[50:51], v55 offset0:115 offset1:123
	s_waitcnt lgkmcnt(3)
	v_bfe_u32 v35, v46, 16, 1
	v_add3_u32 v35, v46, v35, s26
	s_waitcnt lgkmcnt(2)
	v_bfe_u32 v37, v42, 16, 1
	ds_read2_b32 v[60:61], v55 offset0:148 offset1:156
	v_lshrrev_b32_e32 v35, 16, v35
	v_add3_u32 v37, v42, v37, s26
	ds_read2_b32 v[62:63], v55 offset0:181 offset1:189
	v_and_or_b32 v38, v37, s27, v35
	s_waitcnt lgkmcnt(3)
	v_bfe_u32 v35, v48, 16, 1
	v_add3_u32 v35, v48, v35, s26
	s_waitcnt lgkmcnt(2)
	v_bfe_u32 v37, v50, 16, 1
	ds_read2_b32 v[64:65], v55 offset0:214 offset1:222
	v_lshrrev_b32_e32 v35, 16, v35
	v_add3_u32 v37, v50, v37, s26
	ds_read2_b32 v[66:67], v55 offset0:247 offset1:255
	v_and_or_b32 v39, v37, s27, v35
	s_waitcnt lgkmcnt(3)
	v_bfe_u32 v35, v60, 16, 1
	v_add3_u32 v35, v60, v35, s26
	s_waitcnt lgkmcnt(2)
	v_bfe_u32 v37, v62, 16, 1
	v_lshrrev_b32_e32 v35, 16, v35
	v_add3_u32 v37, v62, v37, s26
	v_and_or_b32 v40, v37, s27, v35
	s_waitcnt lgkmcnt(1)
	v_bfe_u32 v35, v64, 16, 1
	v_add3_u32 v35, v64, v35, s26
	s_waitcnt lgkmcnt(0)
	v_bfe_u32 v37, v66, 16, 1
	v_lshrrev_b32_e32 v35, 16, v35
	v_add3_u32 v37, v66, v37, s26
	v_add_u32_e32 v68, s12, v57
	v_and_or_b32 v41, v37, s27, v35
	v_ashrrev_i32_e32 v69, 31, v68
	v_bfe_u32 v35, v47, 16, 1
	v_lshlrev_b64 v[68:69], 11, v[68:69]
	v_add3_u32 v35, v47, v35, s26
	v_bfe_u32 v37, v43, 16, 1
	v_lshl_add_u64 v[68:69], v[44:45], 0, v[68:69]
	v_lshrrev_b32_e32 v35, 16, v35
	v_add3_u32 v37, v43, v37, s26
	global_store_dwordx4 v[68:69], v[38:41], off
	v_add_u32_e32 v42, s12, v58
	v_ashrrev_i32_e32 v43, 31, v42
	v_and_or_b32 v38, v37, s27, v35
	v_bfe_u32 v35, v49, 16, 1
	v_add3_u32 v35, v49, v35, s26
	v_bfe_u32 v37, v51, 16, 1
	v_lshrrev_b32_e32 v35, 16, v35
	v_add3_u32 v37, v51, v37, s26
	v_and_or_b32 v39, v37, s27, v35
	v_bfe_u32 v35, v61, 16, 1
	v_add3_u32 v35, v61, v35, s26
	v_bfe_u32 v37, v63, 16, 1
	v_lshrrev_b32_e32 v35, 16, v35
	v_add3_u32 v37, v63, v37, s26
	v_and_or_b32 v40, v37, s27, v35
	v_bfe_u32 v35, v65, 16, 1
	v_add3_u32 v35, v65, v35, s26
	v_bfe_u32 v37, v67, 16, 1
	v_lshrrev_b32_e32 v35, 16, v35
	v_add3_u32 v37, v67, v37, s26
	v_lshlrev_b64 v[42:43], 11, v[42:43]
	v_and_or_b32 v41, v37, s27, v35
	v_lshl_add_u64 v[42:43], v[44:45], 0, v[42:43]
	global_store_dwordx4 v[42:43], v[38:41], off
	s_waitcnt lgkmcnt(0)

.LBB0_45:
	s_lshl_b32 s18, s13, 1
	s_lshl_b32 s19, s2, 1
	v_add_u32_e32 v60, s18, v40
	v_add_u32_e32 v59, s19, v35
	v_add_u32_e32 v66, s19, v37
	v_add_u32_e32 v64, s18, v42
	v_add_u32_e32 v70, s19, v41
	v_add_u32_e32 v68, s18, v44
	v_add_u32_e32 v74, s19, v43
	v_add_u32_e32 v72, s18, v46
	v_add_u32_e32 v78, s19, v45
	v_add_u32_e32 v76, s18, v48
	v_add_u32_e32 v82, s19, v47
	v_add_u32_e32 v80, s18, v50
	v_add_u32_e32 v86, s19, v49
	v_add_u32_e32 v84, s18, v52
	v_add_u32_e32 v90, s19, v51
	v_add_u32_e32 v88, s18, v54
	v_mad_i64_i32 v[60:61], s[16:17], v60, s28, v[38:39]
	v_mad_i64_i32 v[62:63], s[16:17], v59, s28, v[38:39]
	v_mad_i64_i32 v[64:65], s[16:17], v64, s28, v[38:39]
	v_mad_i64_i32 v[66:67], s[16:17], v66, s28, v[38:39]
	v_mad_i64_i32 v[68:69], s[16:17], v68, s28, v[38:39]
	v_mad_i64_i32 v[70:71], s[16:17], v70, s28, v[38:39]
	v_mad_i64_i32 v[72:73], s[16:17], v72, s28, v[38:39]
	v_mad_i64_i32 v[74:75], s[16:17], v74, s28, v[38:39]
	v_mad_i64_i32 v[76:77], s[16:17], v76, s28, v[38:39]
	v_mad_i64_i32 v[78:79], s[16:17], v78, s28, v[38:39]
	v_mad_i64_i32 v[80:81], s[16:17], v80, s28, v[38:39]
	v_mad_i64_i32 v[82:83], s[16:17], v82, s28, v[38:39]
	v_mad_i64_i32 v[84:85], s[16:17], v84, s28, v[38:39]
	v_mad_i64_i32 v[86:87], s[16:17], v86, s28, v[38:39]
	v_mad_i64_i32 v[88:89], s[16:17], v88, s28, v[38:39]
	v_mad_i64_i32 v[90:91], s[16:17], v90, s28, v[38:39]
	global_load_dword v59, v[60:61], off
	global_load_dword v92, v[62:63], off
	global_load_dword v93, v[64:65], off
	global_load_dword v94, v[66:67], off
	global_load_dword v95, v[68:69], off
	global_load_dword v96, v[70:71], off
	global_load_dword v97, v[72:73], off
	global_load_dword v98, v[74:75], off
	global_load_dword v99, v[76:77], off
	global_load_dword v100, v[78:79], off
	global_load_dword v101, v[80:81], off
	global_load_dword v102, v[82:83], off
	global_load_dword v103, v[84:85], off
	global_load_dword v104, v[86:87], off
	global_load_dword v105, v[88:89], off
	global_load_dword v106, v[90:91], off
	s_add_i32 s13, s13, 16
	s_add_i32 s2, s2, 16
	s_add_i32 s15, s15, -16
	s_lshl_b32 s40, s13, 1
	s_lshl_b32 s41, s2, 1
	v_add_u32_e32 v160, s40, v40
	v_add_u32_e32 v159, s41, v35
	v_add_u32_e32 v166, s41, v37
	v_add_u32_e32 v164, s40, v42
	v_add_u32_e32 v170, s41, v41
	v_add_u32_e32 v168, s40, v44
	v_add_u32_e32 v174, s41, v43
	v_add_u32_e32 v172, s40, v46
	v_add_u32_e32 v178, s41, v45
	v_add_u32_e32 v176, s40, v48
	v_add_u32_e32 v182, s41, v47
	v_add_u32_e32 v180, s40, v50
	v_add_u32_e32 v186, s41, v49
	v_add_u32_e32 v184, s40, v52
	v_add_u32_e32 v190, s41, v51
	v_add_u32_e32 v188, s40, v54
	v_mad_i64_i32 v[160:161], s[16:17], v160, s28, v[38:39]
	v_mad_i64_i32 v[162:163], s[16:17], v159, s28, v[38:39]
	v_mad_i64_i32 v[164:165], s[16:17], v164, s28, v[38:39]
	v_mad_i64_i32 v[166:167], s[16:17], v166, s28, v[38:39]
	v_mad_i64_i32 v[168:169], s[16:17], v168, s28, v[38:39]
	v_mad_i64_i32 v[170:171], s[16:17], v170, s28, v[38:39]
	v_mad_i64_i32 v[172:173], s[16:17], v172, s28, v[38:39]
	v_mad_i64_i32 v[174:175], s[16:17], v174, s28, v[38:39]
	v_mad_i64_i32 v[176:177], s[16:17], v176, s28, v[38:39]
	v_mad_i64_i32 v[178:179], s[16:17], v178, s28, v[38:39]
	v_mad_i64_i32 v[180:181], s[16:17], v180, s28, v[38:39]
	v_mad_i64_i32 v[182:183], s[16:17], v182, s28, v[38:39]
	v_mad_i64_i32 v[184:185], s[16:17], v184, s28, v[38:39]
	v_mad_i64_i32 v[186:187], s[16:17], v186, s28, v[38:39]
	v_mad_i64_i32 v[188:189], s[16:17], v188, s28, v[38:39]
	v_mad_i64_i32 v[190:191], s[16:17], v190, s28, v[38:39]
	global_load_dword v159, v[160:161], off
	global_load_dword v192, v[162:163], off
	global_load_dword v193, v[164:165], off
	global_load_dword v194, v[166:167], off
	global_load_dword v195, v[168:169], off
	global_load_dword v196, v[170:171], off
	global_load_dword v197, v[172:173], off
	global_load_dword v198, v[174:175], off
	global_load_dword v199, v[176:177], off
	global_load_dword v200, v[178:179], off
	global_load_dword v201, v[180:181], off
	global_load_dword v202, v[182:183], off
	global_load_dword v203, v[184:185], off
	global_load_dword v204, v[186:187], off
	global_load_dword v205, v[188:189], off
	global_load_dword v206, v[190:191], off
	s_add_i32 s13, s13, 16
	s_add_i32 s2, s2, 16
	s_add_i32 s15, s15, -16
	v_add_u32_e32 v60, s18, v0
	v_add_u32_e32 v62, s19, v1
	v_add_u32_e32 v66, s19, v21
	v_add_u32_e32 v64, s18, v22
	v_add_u32_e32 v70, s19, v23
	v_add_u32_e32 v68, s18, v24
	v_add_u32_e32 v74, s19, v25
	v_add_u32_e32 v72, s18, v26
	v_add_u32_e32 v78, s19, v27
	v_add_u32_e32 v76, s18, v28
	v_add_u32_e32 v82, s19, v29
	v_add_u32_e32 v80, s18, v30
	v_add_u32_e32 v86, s19, v31
	v_add_u32_e32 v84, s18, v32
	v_add_u32_e32 v90, s19, v33
	v_add_u32_e32 v88, s18, v34
	v_mad_u64_u32 v[60:61], s[16:17], v60, s24, v[20:21]
	v_mad_u64_u32 v[62:63], s[16:17], v62, s24, v[20:21]
	v_mad_u64_u32 v[64:65], s[16:17], v64, s24, v[20:21]
	v_mad_u64_u32 v[66:67], s[16:17], v66, s24, v[20:21]
	v_mad_u64_u32 v[68:69], s[16:17], v68, s24, v[20:21]
	v_mad_u64_u32 v[70:71], s[16:17], v70, s24, v[20:21]
	v_mad_u64_u32 v[72:73], s[16:17], v72, s24, v[20:21]
	v_mad_u64_u32 v[74:75], s[16:17], v74, s24, v[20:21]
	v_mad_u64_u32 v[76:77], s[16:17], v76, s24, v[20:21]
	v_mad_u64_u32 v[78:79], s[16:17], v78, s24, v[20:21]
	v_mad_u64_u32 v[80:81], s[16:17], v80, s24, v[20:21]
	v_mad_u64_u32 v[82:83], s[16:17], v82, s24, v[20:21]
	v_mad_u64_u32 v[84:85], s[16:17], v84, s24, v[20:21]
	v_mad_u64_u32 v[86:87], s[16:17], v86, s24, v[20:21]
	v_mad_u64_u32 v[88:89], s[16:17], v88, s24, v[20:21]
	v_mad_u64_u32 v[90:91], s[16:17], v90, s24, v[20:21]
	s_waitcnt vmcnt(31)
	ds_write_b32 v60, v59
	s_waitcnt vmcnt(30)
	ds_write_b32 v62, v92
	s_waitcnt vmcnt(29)
	ds_write_b32 v64, v93
	s_waitcnt vmcnt(28)
	ds_write_b32 v66, v94
	s_waitcnt vmcnt(27)
	ds_write_b32 v68, v95
	s_waitcnt vmcnt(26)
	ds_write_b32 v70, v96
	s_waitcnt vmcnt(25)
	ds_write_b32 v72, v97
	s_waitcnt vmcnt(24)
	ds_write_b32 v74, v98
	s_waitcnt vmcnt(23)
	ds_write_b32 v76, v99
	s_waitcnt vmcnt(22)
	ds_write_b32 v78, v100
	s_waitcnt vmcnt(21)
	ds_write_b32 v80, v101
	s_waitcnt vmcnt(20)
	ds_write_b32 v82, v102
	s_waitcnt vmcnt(19)
	ds_write_b32 v84, v103
	s_waitcnt vmcnt(18)
	ds_write_b32 v86, v104
	s_waitcnt vmcnt(17)
	ds_write_b32 v88, v105
	s_waitcnt vmcnt(16)
	ds_write_b32 v90, v106
	v_add_u32_e32 v160, s40, v0
	v_add_u32_e32 v162, s41, v1
	v_add_u32_e32 v166, s41, v21
	v_add_u32_e32 v164, s40, v22
	v_add_u32_e32 v170, s41, v23
	v_add_u32_e32 v168, s40, v24
	v_add_u32_e32 v174, s41, v25
	v_add_u32_e32 v172, s40, v26
	v_add_u32_e32 v178, s41, v27
	v_add_u32_e32 v176, s40, v28
	v_add_u32_e32 v182, s41, v29
	v_add_u32_e32 v180, s40, v30
	v_add_u32_e32 v186, s41, v31
	v_add_u32_e32 v184, s40, v32
	v_add_u32_e32 v190, s41, v33
	v_add_u32_e32 v188, s40, v34
	v_mad_u64_u32 v[160:161], s[16:17], v160, s24, v[20:21]
	v_mad_u64_u32 v[162:163], s[16:17], v162, s24, v[20:21]
	v_mad_u64_u32 v[164:165], s[16:17], v164, s24, v[20:21]
	v_mad_u64_u32 v[166:167], s[16:17], v166, s24, v[20:21]
	v_mad_u64_u32 v[168:169], s[16:17], v168, s24, v[20:21]
	v_mad_u64_u32 v[170:171], s[16:17], v170, s24, v[20:21]
	v_mad_u64_u32 v[172:173], s[16:17], v172, s24, v[20:21]
	v_mad_u64_u32 v[174:175], s[16:17], v174, s24, v[20:21]
	v_mad_u64_u32 v[176:177], s[16:17], v176, s24, v[20:21]
	v_mad_u64_u32 v[178:179], s[16:17], v178, s24, v[20:21]
	v_mad_u64_u32 v[180:181], s[16:17], v180, s24, v[20:21]
	v_mad_u64_u32 v[182:183], s[16:17], v182, s24, v[20:21]
	v_mad_u64_u32 v[184:185], s[16:17], v184, s24, v[20:21]
	v_mad_u64_u32 v[186:187], s[16:17], v186, s24, v[20:21]
	v_mad_u64_u32 v[188:189], s[16:17], v188, s24, v[20:21]
	v_mad_u64_u32 v[190:191], s[16:17], v190, s24, v[20:21]
	s_waitcnt vmcnt(15)
	ds_write_b32 v160, v159
	s_waitcnt vmcnt(14)
	ds_write_b32 v162, v192
	s_waitcnt vmcnt(13)
	ds_write_b32 v164, v193
	s_waitcnt vmcnt(12)
	ds_write_b32 v166, v194
	s_waitcnt vmcnt(11)
	ds_write_b32 v168, v195
	s_waitcnt vmcnt(10)
	ds_write_b32 v170, v196
	s_waitcnt vmcnt(9)
	ds_write_b32 v172, v197
	s_waitcnt vmcnt(8)
	ds_write_b32 v174, v198
	s_waitcnt vmcnt(7)
	ds_write_b32 v176, v199
	s_waitcnt vmcnt(6)
	ds_write_b32 v178, v200
	s_waitcnt vmcnt(5)
	ds_write_b32 v180, v201
	s_waitcnt vmcnt(4)
	ds_write_b32 v182, v202
	s_waitcnt vmcnt(3)
	ds_write_b32 v184, v203
	s_waitcnt vmcnt(2)
	ds_write_b32 v186, v204
	s_waitcnt vmcnt(1)
	ds_write_b32 v188, v205
	s_waitcnt vmcnt(0)
	ds_write_b32 v190, v206
	s_waitcnt lgkmcnt(0)
	ds_read2_b32 v[48:49], v55 offset1:33
	ds_read2_b32 v[46:47], v55 offset0:66 offset1:99
	ds_read2_b32 v[42:43], v55 offset0:132 offset1:165
	ds_read2_b32 v[40:41], v55 offset0:198 offset1:231
	v_add_u32_e32 v35, s12, v53
	v_cmp_lt_i32_e32 vcc, s25, v35
	s_and_saveexec_b64 s[16:17], vcc
	s_xor_b64 s[16:17], exec, s[16:17]
	s_cbranch_execz .LBB0_52
	v_cmp_lt_u32_e32 vcc, s29, v35
	v_lshlrev_b32_e32 v37, 1, v35
	v_and_b32_e32 v35, 0x7f, v35
	s_and_saveexec_b64 s[18:19], vcc
	s_xor_b64 s[18:19], exec, s[18:19]
	v_and_or_b32 v35, v37, s30, v35
	v_add_u32_e32 v44, 0xfffff480, v35
	s_andn2_saveexec_b64 s[18:19], s[18:19]
	v_and_or_b32 v35, v37, s31, v35
	v_add_u32_e32 v44, 0xfffff800, v35
	s_or_b64 exec, exec, s[18:19]
